# exp/cvt of half of each tile's scores moved into the MFMA gaps of the next tile's QK^T (kt-major accumulate order), so P.V gaps carry one exp per two MFMAs
# baseline (speedup 1.0000x reference)
; __device__ __forceinline__ int v_rd_base(int lane) { return ((lane & 3) << 3) | (((lane >> 2) & 3) << 6) | (((lane >> 4) & 1) << 5) | (((lane >> 5) & 1) << 8); }
; #define ATT_WAIT_BAR() asm volatile("s_waitcnt vmcnt(0) lgkmcnt(0)\n\ts_barrier" ::: "memory")
; __device__ __forceinline__ void attn_dma_body(const bf16_t* __restrict__ Qb, int ldq, int tpos0, const float* __restrict__ rope, const float* __restrict__ qgain, ...
;     ...
;   ATT_WAIT_BAR();
;   if (2 < NT) ATT_DMA(2, 2);
;   const int vb0 = (int)(uintptr_t)lds + 16384 + v_rd_base(lane);
;   f32x16 pA0, pA1, pB0, pB1; float mnA, mnB, alA, alB; bf16x8 pa0, pa1, pa2, pa3;
;   qkt(pA0, pA1, (const bf16_t*)lds, qr, r32, hi); partialSM(pA0, pA1, m_reg, mnA, alA);
;   const bool lead = __builtin_amdgcn_readfirstlane(wid) < 4;
.Lf16_noprio:
	s_waitcnt vmcnt(0) lgkmcnt(0)
	s_barrier
	s_add_u32 s2, s38, 0x8000
	s_addc_u32 s3, s39, 0
	s_add_u32 s4, s40, 0x8000
	s_addc_u32 s5, s41, 0
	s_add_i32 s6, s96, 0x10000
	s_add_i32 m0, s96, 0x10000
	s_nop 0
	global_load_lds_dwordx4 v170, s[2:3]
	s_add_i32 m0, s96, 0x12000
	s_nop 0
	global_load_lds_dwordx4 v172, s[2:3]
	s_add_i32 m0, s96, 0x14000
	s_nop 0
	global_load_lds_dwordx4 v171, s[2:3]
	s_add_i32 m0, s96, 0x16000
	s_nop 0
	global_load_lds_dwordx4 v173, s[2:3]
	s_add_u32 s2, s2, 0x4000
	s_addc_u32 s3, s3, 0
	v_add_u32_e32 v187, 0x10000, v183
	v_add_u32_e32 v188, 0x10000, v184
	v_add_u32_e32 v189, 0x10000, v185
	v_add_u32_e32 v190, 0x10000, v186
	v_add_u32_e32 v180, 0x10000, v191
	v_add_u32_e32 v181, 0x10000, v192
	s_mov_b32 s36, 0
	ds_read_b128 v[146:149], v183 offset:0
	ds_read_b128 v[150:153], v184 offset:0
	ds_read_b128 v[154:157], v185 offset:0
	ds_read_b128 v[158:161], v186 offset:0
	ds_read_b128 v[198:201], v183 offset:4096
	ds_read_b128 v[202:205], v184 offset:4096
	ds_read_b128 v[206:209], v185 offset:4096
	ds_read_b128 v[210:213], v186 offset:4096
	s_waitcnt lgkmcnt(6)
	v_mfma_f32_16x16x32_bf16 v[66:69], v[146:149], v[98:101], 0
	v_mfma_f32_16x16x32_bf16 v[70:73], v[146:149], v[114:117], 0
	v_mfma_f32_16x16x32_bf16 v[66:69], v[150:153], v[102:105], v[66:69]
	v_mfma_f32_16x16x32_bf16 v[70:73], v[150:153], v[118:121], v[70:73]
	ds_read_b128 v[146:149], v183 offset:8192
	ds_read_b128 v[150:153], v184 offset:8192
	s_waitcnt lgkmcnt(6)
	v_mfma_f32_16x16x32_bf16 v[66:69], v[154:157], v[106:109], v[66:69]
	v_mfma_f32_16x16x32_bf16 v[70:73], v[154:157], v[122:125], v[70:73]
	v_mfma_f32_16x16x32_bf16 v[66:69], v[158:161], v[110:113], v[66:69]
	v_mfma_f32_16x16x32_bf16 v[70:73], v[158:161], v[126:129], v[70:73]
	ds_read_b128 v[154:157], v185 offset:8192
	ds_read_b128 v[158:161], v186 offset:8192
	s_waitcnt lgkmcnt(6)
	v_mfma_f32_16x16x32_bf16 v[74:77], v[198:201], v[98:101], 0
	v_mfma_f32_16x16x32_bf16 v[78:81], v[198:201], v[114:117], 0
	v_mfma_f32_16x16x32_bf16 v[74:77], v[202:205], v[102:105], v[74:77]
	v_mfma_f32_16x16x32_bf16 v[78:81], v[202:205], v[118:121], v[78:81]
	ds_read_b128 v[198:201], v183 offset:12288
	ds_read_b128 v[202:205], v184 offset:12288
	s_waitcnt lgkmcnt(6)
	v_mfma_f32_16x16x32_bf16 v[74:77], v[206:209], v[106:109], v[74:77]
	v_mfma_f32_16x16x32_bf16 v[78:81], v[206:209], v[122:125], v[78:81]
	v_mfma_f32_16x16x32_bf16 v[74:77], v[210:213], v[110:113], v[74:77]
	v_mfma_f32_16x16x32_bf16 v[78:81], v[210:213], v[126:129], v[78:81]
	ds_read_b128 v[206:209], v185 offset:12288
	ds_read_b128 v[210:213], v186 offset:12288
	s_waitcnt lgkmcnt(6)
	v_mfma_f32_16x16x32_bf16 v[82:85], v[146:149], v[98:101], 0
	v_mfma_f32_16x16x32_bf16 v[86:89], v[146:149], v[114:117], 0
	v_mfma_f32_16x16x32_bf16 v[82:85], v[150:153], v[102:105], v[82:85]
	v_mfma_f32_16x16x32_bf16 v[86:89], v[150:153], v[118:121], v[86:89]
	s_waitcnt lgkmcnt(4)
	v_mfma_f32_16x16x32_bf16 v[82:85], v[154:157], v[106:109], v[82:85]
	v_mfma_f32_16x16x32_bf16 v[86:89], v[154:157], v[122:125], v[86:89]
	v_mfma_f32_16x16x32_bf16 v[82:85], v[158:161], v[110:113], v[82:85]
	v_mfma_f32_16x16x32_bf16 v[86:89], v[158:161], v[126:129], v[86:89]
	s_waitcnt lgkmcnt(2)
	v_mfma_f32_16x16x32_bf16 v[90:93], v[198:201], v[98:101], 0
	v_mfma_f32_16x16x32_bf16 v[94:97], v[198:201], v[114:117], 0
	v_mfma_f32_16x16x32_bf16 v[90:93], v[202:205], v[102:105], v[90:93]
	v_mfma_f32_16x16x32_bf16 v[94:97], v[202:205], v[118:121], v[94:97]
	s_waitcnt lgkmcnt(0)
	v_mfma_f32_16x16x32_bf16 v[90:93], v[206:209], v[106:109], v[90:93]
	v_mfma_f32_16x16x32_bf16 v[94:97], v[206:209], v[122:125], v[94:97]
	v_mfma_f32_16x16x32_bf16 v[90:93], v[210:213], v[110:113], v[90:93]
	v_mfma_f32_16x16x32_bf16 v[94:97], v[210:213], v[126:129], v[94:97]
	s_nop 7
	s_nop 7
	v_exp_f32_e32 v66, v66
	v_exp_f32_e32 v67, v67
	v_exp_f32_e32 v68, v68
	v_exp_f32_e32 v69, v69
	v_exp_f32_e32 v70, v70
	v_exp_f32_e32 v71, v71
	v_exp_f32_e32 v72, v72
	v_exp_f32_e32 v73, v73
	v_exp_f32_e32 v74, v74
	v_exp_f32_e32 v75, v75
	v_exp_f32_e32 v76, v76
	v_exp_f32_e32 v77, v77
	v_exp_f32_e32 v78, v78
	v_exp_f32_e32 v79, v79
	v_exp_f32_e32 v80, v80
	v_exp_f32_e32 v81, v81
	v_cvt_pk_bf16_f32 v130, v66, v67
	v_cvt_pk_bf16_f32 v131, v68, v69
	v_cvt_pk_bf16_f32 v132, v74, v75
	v_cvt_pk_bf16_f32 v133, v76, v77
	v_cvt_pk_bf16_f32 v138, v70, v71
	v_cvt_pk_bf16_f32 v139, v72, v73
	v_cvt_pk_bf16_f32 v140, v78, v79
	v_cvt_pk_bf16_f32 v141, v80, v81
	s_mov_b32 s97, 1
	s_cmp_lt_u32 s42, 4
	s_cbranch_scc1 .Lf16_L_loop
	.p2align 6
; #define SBAR() __builtin_amdgcn_sched_barrier(0)
; #define RESC(a) do { if (__any((a) < 1.f)) { if (hi == 0) al_l[r32] = (a); asm volatile("s_waitcnt lgkmcnt(0)" ::: "memory"); \
;     for (int d = 0; d < 4; ++d) for (int r = 0; r < 16; ++r) o[d][r] *= al_l[crow(r, hi)]; } } while (0)
; #define RESC(a) do { if (__any((a) < 1.f)) { if (hi == 0) al_l[r32] = (a); asm volatile("s_waitcnt lgkmcnt(0)" ::: "memory"); \
;     for (int d = 0; d < 4; ++d) for (int r = 0; r < 16; ++r) o[d][r] *= al_l[crow(r, hi)]; } } while (0)
; #define ATT_SYNC(jn) do { ATT_WAIT_BAR(); if ((jn) < NT) ATT_DMA((jn), (jn) & 3); } while (0)
; __device__ __forceinline__ void attn_dma_body(const bf16_t* __restrict__ Qb, int ldq, int tpos0, const float* __restrict__ rope, const float* __restrict__ qgain, ...
;     ...
;   for (int j = 1; j + 1 < NT; j += 2) {
;     { SBAR(); qkt(pB0, pB1, (const bf16_t*)(lds + (j & 3) * SHM_SLOT), qr, r32, hi);
;       finishSM(pA0, pA1, alA, l_reg, pa0, pa1, pa2, pa3); s16x4 va[8]; pv_rd<0>(va, vb0 + ((j - 1) & 3) * (int)SHM_SLOT); SBAR();
;       if (!lead) ATT_SYNC(j + 2);
;       pv_d0_pre(o, vb0 + ((j - 1) & 3) * (int)SHM_SLOT, va, pa0, pa1, pa2, pa3); partialSM(pB0, pB1, m_reg, mnB, alB);
;       if (lead) ATT_SYNC(j + 2);
;       RESC(alB); }
;     { SBAR(); qkt(pA0, pA1, (const bf16_t*)(lds + ((j + 1) & 3) * SHM_SLOT), qr, r32, hi);
;       finishSM(pB0, pB1, alB, l_reg, pa0, pa1, pa2, pa3); s16x4 va[8]; pv_rd<0>(va, vb0 + (j & 3) * (int)SHM_SLOT); SBAR();
;       if (!lead) ATT_SYNC(j + 3);
;       pv_d0_pre(o, vb0 + (j & 3) * (int)SHM_SLOT, va, pa0, pa1, pa2, pa3); partialSM(pA0, pA1, m_reg, mnA, alA);
;       if (lead) ATT_SYNC(j + 3);
;       RESC(alA); }
;   }
.Lf16_N_loop:
	ds_read_b128 v[146:149], v183 offset:32768
	ds_read_b128 v[150:153], v184 offset:32768
	ds_read_b128 v[154:157], v185 offset:32768
	ds_read_b128 v[158:161], v186 offset:32768
	ds_read_b128 v[198:201], v183 offset:36864
	ds_read_b128 v[202:205], v184 offset:36864
	ds_read_b128 v[206:209], v185 offset:36864
	ds_read_b128 v[210:213], v186 offset:36864
	s_waitcnt lgkmcnt(6)
	v_mfma_f32_16x16x32_bf16 v[66:69], v[146:149], v[98:101], 0
	v_exp_f32_e32 v82, v82
	v_mfma_f32_16x16x32_bf16 v[70:73], v[146:149], v[114:117], 0
	v_exp_f32_e32 v83, v83
	v_mfma_f32_16x16x32_bf16 v[66:69], v[150:153], v[102:105], v[66:69]
	v_exp_f32_e32 v84, v84
	v_mfma_f32_16x16x32_bf16 v[70:73], v[150:153], v[118:121], v[70:73]
	v_exp_f32_e32 v85, v85
	ds_read_b128 v[146:149], v183 offset:40960
	ds_read_b128 v[150:153], v184 offset:40960
	s_waitcnt lgkmcnt(6)
	v_mfma_f32_16x16x32_bf16 v[66:69], v[154:157], v[106:109], v[66:69]
	v_exp_f32_e32 v86, v86
	v_mfma_f32_16x16x32_bf16 v[70:73], v[154:157], v[122:125], v[70:73]
	v_exp_f32_e32 v87, v87
	v_mfma_f32_16x16x32_bf16 v[66:69], v[158:161], v[110:113], v[66:69]
	v_exp_f32_e32 v88, v88
	v_mfma_f32_16x16x32_bf16 v[70:73], v[158:161], v[126:129], v[70:73]
	v_exp_f32_e32 v89, v89
	ds_read_b128 v[154:157], v185 offset:40960
	ds_read_b128 v[158:161], v186 offset:40960
	s_waitcnt lgkmcnt(6)
	v_mfma_f32_16x16x32_bf16 v[74:77], v[198:201], v[98:101], 0
	v_exp_f32_e32 v90, v90
	v_mfma_f32_16x16x32_bf16 v[78:81], v[198:201], v[114:117], 0
	v_exp_f32_e32 v91, v91
	v_cvt_pk_bf16_f32 v134, v82, v83
	v_mfma_f32_16x16x32_bf16 v[74:77], v[202:205], v[102:105], v[74:77]
	v_exp_f32_e32 v92, v92
	v_cvt_pk_bf16_f32 v135, v84, v85
	v_mfma_f32_16x16x32_bf16 v[78:81], v[202:205], v[118:121], v[78:81]
	v_exp_f32_e32 v93, v93
	v_cvt_pk_bf16_f32 v142, v86, v87
	ds_read_b128 v[198:201], v183 offset:45056
	ds_read_b128 v[202:205], v184 offset:45056
	s_waitcnt lgkmcnt(6)
	v_mfma_f32_16x16x32_bf16 v[74:77], v[206:209], v[106:109], v[74:77]
	v_exp_f32_e32 v94, v94
	v_cvt_pk_bf16_f32 v143, v88, v89
	v_mfma_f32_16x16x32_bf16 v[78:81], v[206:209], v[122:125], v[78:81]
	v_exp_f32_e32 v95, v95
	v_mfma_f32_16x16x32_bf16 v[74:77], v[210:213], v[110:113], v[74:77]
	v_exp_f32_e32 v96, v96
	v_mfma_f32_16x16x32_bf16 v[78:81], v[210:213], v[126:129], v[78:81]
	v_exp_f32_e32 v97, v97
	ds_read_b128 v[206:209], v185 offset:45056
	ds_read_b128 v[210:213], v186 offset:45056
	s_waitcnt lgkmcnt(6)
	v_mfma_f32_16x16x32_bf16 v[82:85], v[146:149], v[98:101], 0
	v_mfma_f32_16x16x32_bf16 v[86:89], v[146:149], v[114:117], 0
	v_cvt_pk_bf16_f32 v136, v90, v91
	v_mfma_f32_16x16x32_bf16 v[82:85], v[150:153], v[102:105], v[82:85]
	v_cvt_pk_bf16_f32 v137, v92, v93
	v_mfma_f32_16x16x32_bf16 v[86:89], v[150:153], v[118:121], v[86:89]
	v_cvt_pk_bf16_f32 v144, v94, v95
	s_waitcnt lgkmcnt(4)
	v_mfma_f32_16x16x32_bf16 v[82:85], v[154:157], v[106:109], v[82:85]
	v_cvt_pk_bf16_f32 v145, v96, v97
	v_mfma_f32_16x16x32_bf16 v[86:89], v[154:157], v[122:125], v[86:89]
	v_mfma_f32_16x16x32_bf16 v[82:85], v[158:161], v[110:113], v[82:85]
	v_mfma_f32_16x16x32_bf16 v[86:89], v[158:161], v[126:129], v[86:89]
	s_waitcnt lgkmcnt(2)
	v_mfma_f32_16x16x32_bf16 v[90:93], v[198:201], v[98:101], 0
	v_mfma_f32_16x16x32_bf16 v[94:97], v[198:201], v[114:117], 0
	v_mfma_f32_16x16x32_bf16 v[90:93], v[202:205], v[102:105], v[90:93]
	v_mfma_f32_16x16x32_bf16 v[94:97], v[202:205], v[118:121], v[94:97]
	ds_read_b64_tr_b16 v[214:215], v191 offset:0
	ds_read_b64_tr_b16 v[216:217], v191 offset:4096
	ds_read_b64_tr_b16 v[218:219], v192 offset:0
	ds_read_b64_tr_b16 v[220:221], v192 offset:4096
	ds_read_b64_tr_b16 v[222:223], v191 offset:512
	ds_read_b64_tr_b16 v[224:225], v191 offset:4608
	ds_read_b64_tr_b16 v[226:227], v192 offset:512
	ds_read_b64_tr_b16 v[228:229], v192 offset:4608
	ds_read_b64_tr_b16 v[230:231], v191 offset:1024
	ds_read_b64_tr_b16 v[232:233], v191 offset:5120
	ds_read_b64_tr_b16 v[234:235], v192 offset:1024
	ds_read_b64_tr_b16 v[236:237], v192 offset:5120
	s_waitcnt lgkmcnt(12)
	v_mfma_f32_16x16x32_bf16 v[90:93], v[206:209], v[106:109], v[90:93]
	v_mfma_f32_16x16x32_bf16 v[94:97], v[206:209], v[122:125], v[94:97]
	v_mfma_f32_16x16x32_bf16 v[90:93], v[210:213], v[110:113], v[90:93]
	v_mfma_f32_16x16x32_bf16 v[94:97], v[210:213], v[126:129], v[94:97]
	s_waitcnt vmcnt(0) lgkmcnt(0)
	s_barrier
	s_cmp_ge_u32 s97, 130
	s_cbranch_scc1 .Lf16_se_N0
	s_add_i32 m0, s96, 0x18000
	s_nop 0
	global_load_lds_dwordx4 v170, s[2:3]
	s_add_i32 m0, s96, 0x1a000
	s_nop 0
	global_load_lds_dwordx4 v172, s[2:3]
	s_add_i32 m0, s96, 0x1c000
	s_nop 0
	global_load_lds_dwordx4 v171, s[2:3]
	s_add_i32 m0, s96, 0x1e000
	s_nop 0
	global_load_lds_dwordx4 v173, s[2:3]
	s_add_u32 s2, s2, 0x4000
	s_addc_u32 s3, s3, 0
; #define SBAR() __builtin_amdgcn_sched_barrier(0)
; #define RESC(a) do { if (__any((a) < 1.f)) { if (hi == 0) al_l[r32] = (a); asm volatile("s_waitcnt lgkmcnt(0)" ::: "memory"); \
;     for (int d = 0; d < 4; ++d) for (int r = 0; r < 16; ++r) o[d][r] *= al_l[crow(r, hi)]; } } while (0)
; #define RESC(a) do { if (__any((a) < 1.f)) { if (hi == 0) al_l[r32] = (a); asm volatile("s_waitcnt lgkmcnt(0)" ::: "memory"); \
;     for (int d = 0; d < 4; ++d) for (int r = 0; r < 16; ++r) o[d][r] *= al_l[crow(r, hi)]; } } while (0)
; #define ATT_SYNC(jn) do { ATT_WAIT_BAR(); if ((jn) < NT) ATT_DMA((jn), (jn) & 3); } while (0)
; __device__ __forceinline__ void attn_dma_body(const bf16_t* __restrict__ Qb, int ldq, int tpos0, const float* __restrict__ rope, const float* __restrict__ qgain, ...
;     ...
;   for (int j = 1; j + 1 < NT; j += 2) {
;     { SBAR(); qkt(pB0, pB1, (const bf16_t*)(lds + (j & 3) * SHM_SLOT), qr, r32, hi);
;       finishSM(pA0, pA1, alA, l_reg, pa0, pa1, pa2, pa3); s16x4 va[8]; pv_rd<0>(va, vb0 + ((j - 1) & 3) * (int)SHM_SLOT); SBAR();
;       if (!lead) ATT_SYNC(j + 2);
;       pv_d0_pre(o, vb0 + ((j - 1) & 3) * (int)SHM_SLOT, va, pa0, pa1, pa2, pa3); partialSM(pB0, pB1, m_reg, mnB, alB);
;       if (lead) ATT_SYNC(j + 2);
;       RESC(alB); }
;     { SBAR(); qkt(pA0, pA1, (const bf16_t*)(lds + ((j + 1) & 3) * SHM_SLOT), qr, r32, hi);
;       finishSM(pB0, pB1, alB, l_reg, pa0, pa1, pa2, pa3); s16x4 va[8]; pv_rd<0>(va, vb0 + (j & 3) * (int)SHM_SLOT); SBAR();
;       if (!lead) ATT_SYNC(j + 3);
;       pv_d0_pre(o, vb0 + (j & 3) * (int)SHM_SLOT, va, pa0, pa1, pa2, pa3); partialSM(pA0, pA1, m_reg, mnA, alA);
;       if (lead) ATT_SYNC(j + 3);
;       RESC(alA); }
;   }
.Lf16_se_N0:
	s_waitcnt lgkmcnt(8)
	v_mfma_f32_16x16x32_bf16 v[2:5], v[214:217], v[130:133], v[2:5]
	v_mfma_f32_16x16x32_bf16 v[6:9], v[214:217], v[138:141], v[6:9]
	v_exp_f32_e32 v66, v66
	v_mfma_f32_16x16x32_bf16 v[10:13], v[218:221], v[130:133], v[10:13]
	v_mfma_f32_16x16x32_bf16 v[14:17], v[218:221], v[138:141], v[14:17]
	v_exp_f32_e32 v67, v67
	ds_read_b64_tr_b16 v[238:239], v191 offset:1536
	ds_read_b64_tr_b16 v[240:241], v191 offset:5632
	ds_read_b64_tr_b16 v[242:243], v192 offset:1536
	ds_read_b64_tr_b16 v[244:245], v192 offset:5632
	s_waitcnt lgkmcnt(8)
	v_mfma_f32_16x16x32_bf16 v[18:21], v[222:225], v[130:133], v[18:21]
	v_mfma_f32_16x16x32_bf16 v[22:25], v[222:225], v[138:141], v[22:25]
	v_exp_f32_e32 v68, v68
	v_mfma_f32_16x16x32_bf16 v[26:29], v[226:229], v[130:133], v[26:29]
	v_mfma_f32_16x16x32_bf16 v[30:33], v[226:229], v[138:141], v[30:33]
	v_exp_f32_e32 v69, v69
	v_mfma_f32_16x16x32_bf16 v[246:249], v[194:197], v[130:133], v[246:249]
	ds_read_b64_tr_b16 v[214:215], v191 offset:8192
	ds_read_b64_tr_b16 v[216:217], v191 offset:12288
	ds_read_b64_tr_b16 v[218:219], v192 offset:8192
	ds_read_b64_tr_b16 v[220:221], v192 offset:12288
	s_waitcnt lgkmcnt(8)
	v_mfma_f32_16x16x32_bf16 v[34:37], v[230:233], v[130:133], v[34:37]
	v_mfma_f32_16x16x32_bf16 v[38:41], v[230:233], v[138:141], v[38:41]
	v_exp_f32_e32 v70, v70
	v_mfma_f32_16x16x32_bf16 v[42:45], v[234:237], v[130:133], v[42:45]
	v_mfma_f32_16x16x32_bf16 v[46:49], v[234:237], v[138:141], v[46:49]
	v_exp_f32_e32 v71, v71
	ds_read_b64_tr_b16 v[222:223], v191 offset:8704
	ds_read_b64_tr_b16 v[224:225], v191 offset:12800
	ds_read_b64_tr_b16 v[226:227], v192 offset:8704
	ds_read_b64_tr_b16 v[228:229], v192 offset:12800
	s_waitcnt lgkmcnt(8)
	v_mfma_f32_16x16x32_bf16 v[50:53], v[238:241], v[130:133], v[50:53]
	v_mfma_f32_16x16x32_bf16 v[54:57], v[238:241], v[138:141], v[54:57]
	v_exp_f32_e32 v72, v72
	v_mfma_f32_16x16x32_bf16 v[58:61], v[242:245], v[130:133], v[58:61]
	v_mfma_f32_16x16x32_bf16 v[62:65], v[242:245], v[138:141], v[62:65]
	v_exp_f32_e32 v73, v73
	v_mfma_f32_16x16x32_bf16 v[252:255], v[194:197], v[138:141], v[252:255]
	ds_read_b64_tr_b16 v[230:231], v191 offset:9216
	ds_read_b64_tr_b16 v[232:233], v191 offset:13312
	ds_read_b64_tr_b16 v[234:235], v192 offset:9216
	ds_read_b64_tr_b16 v[236:237], v192 offset:13312
	s_waitcnt lgkmcnt(8)
	v_mfma_f32_16x16x32_bf16 v[2:5], v[214:217], v[134:137], v[2:5]
	v_mfma_f32_16x16x32_bf16 v[6:9], v[214:217], v[142:145], v[6:9]
	v_exp_f32_e32 v74, v74
	v_mfma_f32_16x16x32_bf16 v[10:13], v[218:221], v[134:137], v[10:13]
	v_mfma_f32_16x16x32_bf16 v[14:17], v[218:221], v[142:145], v[14:17]
	v_exp_f32_e32 v75, v75
	ds_read_b64_tr_b16 v[238:239], v191 offset:9728
	ds_read_b64_tr_b16 v[240:241], v191 offset:13824
	ds_read_b64_tr_b16 v[242:243], v192 offset:9728
	ds_read_b64_tr_b16 v[244:245], v192 offset:13824
	s_waitcnt lgkmcnt(8)
	v_mfma_f32_16x16x32_bf16 v[18:21], v[222:225], v[134:137], v[18:21]
	v_mfma_f32_16x16x32_bf16 v[22:25], v[222:225], v[142:145], v[22:25]
	v_exp_f32_e32 v76, v76
	v_mfma_f32_16x16x32_bf16 v[26:29], v[226:229], v[134:137], v[26:29]
	v_mfma_f32_16x16x32_bf16 v[30:33], v[226:229], v[142:145], v[30:33]
	v_exp_f32_e32 v77, v77
	v_mfma_f32_16x16x32_bf16 v[246:249], v[194:197], v[134:137], v[246:249]
	s_waitcnt lgkmcnt(4)
	v_mfma_f32_16x16x32_bf16 v[34:37], v[230:233], v[134:137], v[34:37]
	v_mfma_f32_16x16x32_bf16 v[38:41], v[230:233], v[142:145], v[38:41]
	v_exp_f32_e32 v78, v78
	v_mfma_f32_16x16x32_bf16 v[42:45], v[234:237], v[134:137], v[42:45]
	v_mfma_f32_16x16x32_bf16 v[46:49], v[234:237], v[142:145], v[46:49]
	v_exp_f32_e32 v79, v79
	s_waitcnt lgkmcnt(0)
	v_mfma_f32_16x16x32_bf16 v[50:53], v[238:241], v[134:137], v[50:53]
	v_mfma_f32_16x16x32_bf16 v[54:57], v[238:241], v[142:145], v[54:57]
	v_exp_f32_e32 v80, v80
	v_mfma_f32_16x16x32_bf16 v[58:61], v[242:245], v[134:137], v[58:61]
	v_mfma_f32_16x16x32_bf16 v[62:65], v[242:245], v[142:145], v[62:65]
	v_exp_f32_e32 v81, v81
	v_mfma_f32_16x16x32_bf16 v[252:255], v[194:197], v[142:145], v[252:255]
	v_cvt_pk_bf16_f32 v130, v66, v67
	v_cvt_pk_bf16_f32 v131, v68, v69
	v_cvt_pk_bf16_f32 v132, v74, v75
	v_cvt_pk_bf16_f32 v133, v76, v77
	v_cvt_pk_bf16_f32 v138, v70, v71
	v_cvt_pk_bf16_f32 v139, v72, v73
	v_cvt_pk_bf16_f32 v140, v78, v79
	v_cvt_pk_bf16_f32 v141, v80, v81
	s_add_i32 s97, s97, 1
	ds_read_b128 v[146:149], v187 offset:0
	ds_read_b128 v[150:153], v188 offset:0
	ds_read_b128 v[154:157], v189 offset:0
	ds_read_b128 v[158:161], v190 offset:0
	ds_read_b128 v[198:201], v187 offset:4096
	ds_read_b128 v[202:205], v188 offset:4096
	ds_read_b128 v[206:209], v189 offset:4096
	ds_read_b128 v[210:213], v190 offset:4096
	s_waitcnt lgkmcnt(6)
	v_mfma_f32_16x16x32_bf16 v[66:69], v[146:149], v[98:101], 0
	v_exp_f32_e32 v82, v82
	v_mfma_f32_16x16x32_bf16 v[70:73], v[146:149], v[114:117], 0
	v_exp_f32_e32 v83, v83
	v_mfma_f32_16x16x32_bf16 v[66:69], v[150:153], v[102:105], v[66:69]
	v_exp_f32_e32 v84, v84
	v_mfma_f32_16x16x32_bf16 v[70:73], v[150:153], v[118:121], v[70:73]
	v_exp_f32_e32 v85, v85
	ds_read_b128 v[146:149], v187 offset:8192
	ds_read_b128 v[150:153], v188 offset:8192
	s_waitcnt lgkmcnt(6)
	v_mfma_f32_16x16x32_bf16 v[66:69], v[154:157], v[106:109], v[66:69]
	v_exp_f32_e32 v86, v86
	v_mfma_f32_16x16x32_bf16 v[70:73], v[154:157], v[122:125], v[70:73]
	v_exp_f32_e32 v87, v87
	v_mfma_f32_16x16x32_bf16 v[66:69], v[158:161], v[110:113], v[66:69]
	v_exp_f32_e32 v88, v88
	v_mfma_f32_16x16x32_bf16 v[70:73], v[158:161], v[126:129], v[70:73]
	v_exp_f32_e32 v89, v89
	ds_read_b128 v[154:157], v189 offset:8192
	ds_read_b128 v[158:161], v190 offset:8192
	s_waitcnt lgkmcnt(6)
; #define SBAR() __builtin_amdgcn_sched_barrier(0)
; #define RESC(a) do { if (__any((a) < 1.f)) { if (hi == 0) al_l[r32] = (a); asm volatile("s_waitcnt lgkmcnt(0)" ::: "memory"); \
;     for (int d = 0; d < 4; ++d) for (int r = 0; r < 16; ++r) o[d][r] *= al_l[crow(r, hi)]; } } while (0)
; #define RESC(a) do { if (__any((a) < 1.f)) { if (hi == 0) al_l[r32] = (a); asm volatile("s_waitcnt lgkmcnt(0)" ::: "memory"); \
;     for (int d = 0; d < 4; ++d) for (int r = 0; r < 16; ++r) o[d][r] *= al_l[crow(r, hi)]; } } while (0)
; #define ATT_SYNC(jn) do { ATT_WAIT_BAR(); if ((jn) < NT) ATT_DMA((jn), (jn) & 3); } while (0)
; __device__ __forceinline__ void attn_dma_body(const bf16_t* __restrict__ Qb, int ldq, int tpos0, const float* __restrict__ rope, const float* __restrict__ qgain, ...
;     ...
;   for (int j = 1; j + 1 < NT; j += 2) {
;     { SBAR(); qkt(pB0, pB1, (const bf16_t*)(lds + (j & 3) * SHM_SLOT), qr, r32, hi);
;       finishSM(pA0, pA1, alA, l_reg, pa0, pa1, pa2, pa3); s16x4 va[8]; pv_rd<0>(va, vb0 + ((j - 1) & 3) * (int)SHM_SLOT); SBAR();
;       if (!lead) ATT_SYNC(j + 2);
;       pv_d0_pre(o, vb0 + ((j - 1) & 3) * (int)SHM_SLOT, va, pa0, pa1, pa2, pa3); partialSM(pB0, pB1, m_reg, mnB, alB);
;       if (lead) ATT_SYNC(j + 2);
;       RESC(alB); }
;     { SBAR(); qkt(pA0, pA1, (const bf16_t*)(lds + ((j + 1) & 3) * SHM_SLOT), qr, r32, hi);
;       finishSM(pB0, pB1, alB, l_reg, pa0, pa1, pa2, pa3); s16x4 va[8]; pv_rd<0>(va, vb0 + (j & 3) * (int)SHM_SLOT); SBAR();
;       if (!lead) ATT_SYNC(j + 3);
;       pv_d0_pre(o, vb0 + (j & 3) * (int)SHM_SLOT, va, pa0, pa1, pa2, pa3); partialSM(pA0, pA1, m_reg, mnA, alA);
;       if (lead) ATT_SYNC(j + 3);
;       RESC(alA); }
;   }
	v_mfma_f32_16x16x32_bf16 v[74:77], v[198:201], v[98:101], 0
	v_exp_f32_e32 v90, v90
	v_mfma_f32_16x16x32_bf16 v[78:81], v[198:201], v[114:117], 0
	v_exp_f32_e32 v91, v91
	v_cvt_pk_bf16_f32 v134, v82, v83
	v_mfma_f32_16x16x32_bf16 v[74:77], v[202:205], v[102:105], v[74:77]
	v_exp_f32_e32 v92, v92
	v_cvt_pk_bf16_f32 v135, v84, v85
	v_mfma_f32_16x16x32_bf16 v[78:81], v[202:205], v[118:121], v[78:81]
	v_exp_f32_e32 v93, v93
	v_cvt_pk_bf16_f32 v142, v86, v87
	ds_read_b128 v[198:201], v187 offset:12288
	ds_read_b128 v[202:205], v188 offset:12288
	s_waitcnt lgkmcnt(6)
	v_mfma_f32_16x16x32_bf16 v[74:77], v[206:209], v[106:109], v[74:77]
	v_exp_f32_e32 v94, v94
	v_cvt_pk_bf16_f32 v143, v88, v89
	v_mfma_f32_16x16x32_bf16 v[78:81], v[206:209], v[122:125], v[78:81]
	v_exp_f32_e32 v95, v95
	v_mfma_f32_16x16x32_bf16 v[74:77], v[210:213], v[110:113], v[74:77]
	v_exp_f32_e32 v96, v96
	v_mfma_f32_16x16x32_bf16 v[78:81], v[210:213], v[126:129], v[78:81]
	v_exp_f32_e32 v97, v97
	ds_read_b128 v[206:209], v189 offset:12288
	ds_read_b128 v[210:213], v190 offset:12288
	s_waitcnt lgkmcnt(6)
	v_mfma_f32_16x16x32_bf16 v[82:85], v[146:149], v[98:101], 0
	v_mfma_f32_16x16x32_bf16 v[86:89], v[146:149], v[114:117], 0
	v_cvt_pk_bf16_f32 v136, v90, v91
	v_mfma_f32_16x16x32_bf16 v[82:85], v[150:153], v[102:105], v[82:85]
	v_cvt_pk_bf16_f32 v137, v92, v93
	v_mfma_f32_16x16x32_bf16 v[86:89], v[150:153], v[118:121], v[86:89]
	v_cvt_pk_bf16_f32 v144, v94, v95
	s_waitcnt lgkmcnt(4)
	v_mfma_f32_16x16x32_bf16 v[82:85], v[154:157], v[106:109], v[82:85]
	v_cvt_pk_bf16_f32 v145, v96, v97
	v_mfma_f32_16x16x32_bf16 v[86:89], v[154:157], v[122:125], v[86:89]
	v_mfma_f32_16x16x32_bf16 v[82:85], v[158:161], v[110:113], v[82:85]
	v_mfma_f32_16x16x32_bf16 v[86:89], v[158:161], v[126:129], v[86:89]
	s_waitcnt lgkmcnt(2)
	v_mfma_f32_16x16x32_bf16 v[90:93], v[198:201], v[98:101], 0
	v_mfma_f32_16x16x32_bf16 v[94:97], v[198:201], v[114:117], 0
	v_mfma_f32_16x16x32_bf16 v[90:93], v[202:205], v[102:105], v[90:93]
	v_mfma_f32_16x16x32_bf16 v[94:97], v[202:205], v[118:121], v[94:97]
	ds_read_b64_tr_b16 v[214:215], v191 offset:32768
	ds_read_b64_tr_b16 v[216:217], v191 offset:36864
	ds_read_b64_tr_b16 v[218:219], v192 offset:32768
	ds_read_b64_tr_b16 v[220:221], v192 offset:36864
	ds_read_b64_tr_b16 v[222:223], v191 offset:33280
	ds_read_b64_tr_b16 v[224:225], v191 offset:37376
	ds_read_b64_tr_b16 v[226:227], v192 offset:33280
	ds_read_b64_tr_b16 v[228:229], v192 offset:37376
	ds_read_b64_tr_b16 v[230:231], v191 offset:33792
	ds_read_b64_tr_b16 v[232:233], v191 offset:37888
	ds_read_b64_tr_b16 v[234:235], v192 offset:33792
	ds_read_b64_tr_b16 v[236:237], v192 offset:37888
	s_waitcnt lgkmcnt(12)
	v_mfma_f32_16x16x32_bf16 v[90:93], v[206:209], v[106:109], v[90:93]
	v_mfma_f32_16x16x32_bf16 v[94:97], v[206:209], v[122:125], v[94:97]
	v_mfma_f32_16x16x32_bf16 v[90:93], v[210:213], v[110:113], v[90:93]
	v_mfma_f32_16x16x32_bf16 v[94:97], v[210:213], v[126:129], v[94:97]
	s_waitcnt vmcnt(0) lgkmcnt(0)
	s_barrier
	s_cmp_ge_u32 s97, 130
	s_cbranch_scc1 .Lf16_se_N1
	s_add_i32 m0, s96, 0x0
	s_nop 0
	global_load_lds_dwordx4 v170, s[2:3]
	s_add_i32 m0, s96, 0x2000
	s_nop 0
	global_load_lds_dwordx4 v172, s[2:3]
	s_add_i32 m0, s96, 0x4000
	s_nop 0
	global_load_lds_dwordx4 v171, s[2:3]
	s_add_i32 m0, s96, 0x6000
	s_nop 0
	global_load_lds_dwordx4 v173, s[2:3]
	s_add_u32 s2, s2, 0x4000
	s_addc_u32 s3, s3, 0
.Lf16_se_N1:
	s_waitcnt lgkmcnt(8)
	v_mfma_f32_16x16x32_bf16 v[2:5], v[214:217], v[130:133], v[2:5]
	v_mfma_f32_16x16x32_bf16 v[6:9], v[214:217], v[138:141], v[6:9]
	v_exp_f32_e32 v66, v66
	v_mfma_f32_16x16x32_bf16 v[10:13], v[218:221], v[130:133], v[10:13]
	v_mfma_f32_16x16x32_bf16 v[14:17], v[218:221], v[138:141], v[14:17]
	v_exp_f32_e32 v67, v67
	ds_read_b64_tr_b16 v[238:239], v191 offset:34304
	ds_read_b64_tr_b16 v[240:241], v191 offset:38400
	ds_read_b64_tr_b16 v[242:243], v192 offset:34304
	ds_read_b64_tr_b16 v[244:245], v192 offset:38400
	s_waitcnt lgkmcnt(8)
	v_mfma_f32_16x16x32_bf16 v[18:21], v[222:225], v[130:133], v[18:21]
	v_mfma_f32_16x16x32_bf16 v[22:25], v[222:225], v[138:141], v[22:25]
	v_exp_f32_e32 v68, v68
	v_mfma_f32_16x16x32_bf16 v[26:29], v[226:229], v[130:133], v[26:29]
	v_mfma_f32_16x16x32_bf16 v[30:33], v[226:229], v[138:141], v[30:33]
	v_exp_f32_e32 v69, v69
	v_mfma_f32_16x16x32_bf16 v[246:249], v[194:197], v[130:133], v[246:249]
	ds_read_b64_tr_b16 v[214:215], v191 offset:40960
	ds_read_b64_tr_b16 v[216:217], v191 offset:45056
	ds_read_b64_tr_b16 v[218:219], v192 offset:40960
	ds_read_b64_tr_b16 v[220:221], v192 offset:45056
	s_waitcnt lgkmcnt(8)
	v_mfma_f32_16x16x32_bf16 v[34:37], v[230:233], v[130:133], v[34:37]
	v_mfma_f32_16x16x32_bf16 v[38:41], v[230:233], v[138:141], v[38:41]
	v_exp_f32_e32 v70, v70
	v_mfma_f32_16x16x32_bf16 v[42:45], v[234:237], v[130:133], v[42:45]
	v_mfma_f32_16x16x32_bf16 v[46:49], v[234:237], v[138:141], v[46:49]
	v_exp_f32_e32 v71, v71
	ds_read_b64_tr_b16 v[222:223], v191 offset:41472
	ds_read_b64_tr_b16 v[224:225], v191 offset:45568
	ds_read_b64_tr_b16 v[226:227], v192 offset:41472
	ds_read_b64_tr_b16 v[228:229], v192 offset:45568
	s_waitcnt lgkmcnt(8)
	v_mfma_f32_16x16x32_bf16 v[50:53], v[238:241], v[130:133], v[50:53]
	v_mfma_f32_16x16x32_bf16 v[54:57], v[238:241], v[138:141], v[54:57]
	v_exp_f32_e32 v72, v72
	v_mfma_f32_16x16x32_bf16 v[58:61], v[242:245], v[130:133], v[58:61]
	v_mfma_f32_16x16x32_bf16 v[62:65], v[242:245], v[138:141], v[62:65]
	v_exp_f32_e32 v73, v73
	v_mfma_f32_16x16x32_bf16 v[252:255], v[194:197], v[138:141], v[252:255]
	ds_read_b64_tr_b16 v[230:231], v191 offset:41984
	ds_read_b64_tr_b16 v[232:233], v191 offset:46080
	ds_read_b64_tr_b16 v[234:235], v192 offset:41984
	ds_read_b64_tr_b16 v[236:237], v192 offset:46080
	s_waitcnt lgkmcnt(8)
; __device__ __forceinline__ void finishSM(f32x16& p0, f32x16& p1, float alpha, float& l_reg, bf16x8& pa0, bf16x8& pa1, bf16x8& pa2, bf16x8& pa3) {
;   for (int r = 0; r < 16; ++r) p1[r] = __builtin_amdgcn_exp2f(p1[r]);
;   float ps = 0; for (int r = 0; r < 16; ++r) ps += p0[r]; for (int r = 0; r < 16; ++r) ps += p1[r];
;   { auto rr = __builtin_amdgcn_permlane32_swap(__float_as_uint(ps), __float_as_uint(ps), false, false);
;     ps = __uint_as_float(rr[0]) + __uint_as_float(rr[1]); }
;   l_reg = l_reg * alpha + ps;
;     ...
;   PK4(p0, 0, pa0); PK4(p0, 8, pa1); PK4(p1, 0, pa2); PK4(p1, 8, pa3);
; __device__ __forceinline__ void qkt(f32x16& p0, f32x16& p1, const bf16_t* Ks, const bf16x8* qr, int r32, int hi) {
;   p0 = f32x16{}; p1 = f32x16{};
;   for (int d0 = 0; d0 < 8; ++d0) { int cb = (d0 * 16 + hi * 8) * 2;
;     bf16x8 b0 = *reinterpret_cast<const bf16x8*>((const char*)Ks + KSWZ(r32, cb));
;     bf16x8 b1 = *reinterpret_cast<const bf16x8*>((const char*)Ks + KSWZ(32 + r32, cb));
;     p0 = __builtin_amdgcn_mfma_f32_32x32x16_bf16(b0, qr[d0], p0, 0, 0, 0);
;     p1 = __builtin_amdgcn_mfma_f32_32x32x16_bf16(b1, qr[d0], p1, 0, 0, 0); }
; }
	v_mfma_f32_16x16x32_bf16 v[2:5], v[214:217], v[134:137], v[2:5]
	v_mfma_f32_16x16x32_bf16 v[6:9], v[214:217], v[142:145], v[6:9]
	v_exp_f32_e32 v74, v74
	v_mfma_f32_16x16x32_bf16 v[10:13], v[218:221], v[134:137], v[10:13]
	v_mfma_f32_16x16x32_bf16 v[14:17], v[218:221], v[142:145], v[14:17]
	v_exp_f32_e32 v75, v75
	ds_read_b64_tr_b16 v[238:239], v191 offset:42496
	ds_read_b64_tr_b16 v[240:241], v191 offset:46592
	ds_read_b64_tr_b16 v[242:243], v192 offset:42496
	ds_read_b64_tr_b16 v[244:245], v192 offset:46592
	s_waitcnt lgkmcnt(8)
	v_mfma_f32_16x16x32_bf16 v[18:21], v[222:225], v[134:137], v[18:21]
	v_mfma_f32_16x16x32_bf16 v[22:25], v[222:225], v[142:145], v[22:25]
	v_exp_f32_e32 v76, v76
	v_mfma_f32_16x16x32_bf16 v[26:29], v[226:229], v[134:137], v[26:29]
	v_mfma_f32_16x16x32_bf16 v[30:33], v[226:229], v[142:145], v[30:33]
	v_exp_f32_e32 v77, v77
	v_mfma_f32_16x16x32_bf16 v[246:249], v[194:197], v[134:137], v[246:249]
	s_waitcnt lgkmcnt(4)
	v_mfma_f32_16x16x32_bf16 v[34:37], v[230:233], v[134:137], v[34:37]
	v_mfma_f32_16x16x32_bf16 v[38:41], v[230:233], v[142:145], v[38:41]
	v_exp_f32_e32 v78, v78
	v_mfma_f32_16x16x32_bf16 v[42:45], v[234:237], v[134:137], v[42:45]
	v_mfma_f32_16x16x32_bf16 v[46:49], v[234:237], v[142:145], v[46:49]
	v_exp_f32_e32 v79, v79
	s_waitcnt lgkmcnt(0)
	v_mfma_f32_16x16x32_bf16 v[50:53], v[238:241], v[134:137], v[50:53]
	v_mfma_f32_16x16x32_bf16 v[54:57], v[238:241], v[142:145], v[54:57]
	v_exp_f32_e32 v80, v80
	v_mfma_f32_16x16x32_bf16 v[58:61], v[242:245], v[134:137], v[58:61]
	v_mfma_f32_16x16x32_bf16 v[62:65], v[242:245], v[142:145], v[62:65]
	v_exp_f32_e32 v81, v81
	v_mfma_f32_16x16x32_bf16 v[252:255], v[194:197], v[142:145], v[252:255]
	v_cvt_pk_bf16_f32 v130, v66, v67
	v_cvt_pk_bf16_f32 v131, v68, v69
	v_cvt_pk_bf16_f32 v132, v74, v75
	v_cvt_pk_bf16_f32 v133, v76, v77
	v_cvt_pk_bf16_f32 v138, v70, v71
	v_cvt_pk_bf16_f32 v139, v72, v73
	v_cvt_pk_bf16_f32 v140, v78, v79
	v_cvt_pk_bf16_f32 v141, v80, v81
	s_add_i32 s97, s97, 1
	ds_read_b128 v[146:149], v187 offset:32768
	ds_read_b128 v[150:153], v188 offset:32768
	ds_read_b128 v[154:157], v189 offset:32768
	ds_read_b128 v[158:161], v190 offset:32768
	ds_read_b128 v[198:201], v187 offset:36864
	ds_read_b128 v[202:205], v188 offset:36864
	ds_read_b128 v[206:209], v189 offset:36864
	ds_read_b128 v[210:213], v190 offset:36864
	s_waitcnt lgkmcnt(6)
	v_mfma_f32_16x16x32_bf16 v[66:69], v[146:149], v[98:101], 0
	v_exp_f32_e32 v82, v82
	v_mfma_f32_16x16x32_bf16 v[70:73], v[146:149], v[114:117], 0
	v_exp_f32_e32 v83, v83
	v_mfma_f32_16x16x32_bf16 v[66:69], v[150:153], v[102:105], v[66:69]
	v_exp_f32_e32 v84, v84
	v_mfma_f32_16x16x32_bf16 v[70:73], v[150:153], v[118:121], v[70:73]
	v_exp_f32_e32 v85, v85
	ds_read_b128 v[146:149], v187 offset:40960
	ds_read_b128 v[150:153], v188 offset:40960
	s_waitcnt lgkmcnt(6)
	v_mfma_f32_16x16x32_bf16 v[66:69], v[154:157], v[106:109], v[66:69]
	v_exp_f32_e32 v86, v86
	v_mfma_f32_16x16x32_bf16 v[70:73], v[154:157], v[122:125], v[70:73]
	v_exp_f32_e32 v87, v87
	v_mfma_f32_16x16x32_bf16 v[66:69], v[158:161], v[110:113], v[66:69]
	v_exp_f32_e32 v88, v88
	v_mfma_f32_16x16x32_bf16 v[70:73], v[158:161], v[126:129], v[70:73]
	v_exp_f32_e32 v89, v89
	ds_read_b128 v[154:157], v189 offset:40960
	ds_read_b128 v[158:161], v190 offset:40960
	s_waitcnt lgkmcnt(6)
	v_mfma_f32_16x16x32_bf16 v[74:77], v[198:201], v[98:101], 0
	v_exp_f32_e32 v90, v90
	v_mfma_f32_16x16x32_bf16 v[78:81], v[198:201], v[114:117], 0
	v_exp_f32_e32 v91, v91
	v_cvt_pk_bf16_f32 v134, v82, v83
	v_mfma_f32_16x16x32_bf16 v[74:77], v[202:205], v[102:105], v[74:77]
	v_exp_f32_e32 v92, v92
	v_cvt_pk_bf16_f32 v135, v84, v85
	v_mfma_f32_16x16x32_bf16 v[78:81], v[202:205], v[118:121], v[78:81]
	v_exp_f32_e32 v93, v93
	v_cvt_pk_bf16_f32 v142, v86, v87
	ds_read_b128 v[198:201], v187 offset:45056
	ds_read_b128 v[202:205], v188 offset:45056
	s_waitcnt lgkmcnt(6)
	v_mfma_f32_16x16x32_bf16 v[74:77], v[206:209], v[106:109], v[74:77]
	v_exp_f32_e32 v94, v94
	v_cvt_pk_bf16_f32 v143, v88, v89
	v_mfma_f32_16x16x32_bf16 v[78:81], v[206:209], v[122:125], v[78:81]
	v_exp_f32_e32 v95, v95
	v_mfma_f32_16x16x32_bf16 v[74:77], v[210:213], v[110:113], v[74:77]
	v_exp_f32_e32 v96, v96
	v_mfma_f32_16x16x32_bf16 v[78:81], v[210:213], v[126:129], v[78:81]
	v_exp_f32_e32 v97, v97
	ds_read_b128 v[206:209], v189 offset:45056
	ds_read_b128 v[210:213], v190 offset:45056
	s_waitcnt lgkmcnt(6)
	v_mfma_f32_16x16x32_bf16 v[82:85], v[146:149], v[98:101], 0
	v_mfma_f32_16x16x32_bf16 v[86:89], v[146:149], v[114:117], 0
	v_cvt_pk_bf16_f32 v136, v90, v91
	v_mfma_f32_16x16x32_bf16 v[82:85], v[150:153], v[102:105], v[82:85]
	v_cvt_pk_bf16_f32 v137, v92, v93
	v_mfma_f32_16x16x32_bf16 v[86:89], v[150:153], v[118:121], v[86:89]
	v_cvt_pk_bf16_f32 v144, v94, v95
	s_waitcnt lgkmcnt(4)
	v_mfma_f32_16x16x32_bf16 v[82:85], v[154:157], v[106:109], v[82:85]
	v_cvt_pk_bf16_f32 v145, v96, v97
	v_mfma_f32_16x16x32_bf16 v[86:89], v[154:157], v[122:125], v[86:89]
	v_mfma_f32_16x16x32_bf16 v[82:85], v[158:161], v[110:113], v[82:85]
	v_mfma_f32_16x16x32_bf16 v[86:89], v[158:161], v[126:129], v[86:89]
	s_waitcnt lgkmcnt(2)
	v_mfma_f32_16x16x32_bf16 v[90:93], v[198:201], v[98:101], 0
	v_mfma_f32_16x16x32_bf16 v[94:97], v[198:201], v[114:117], 0
	v_mfma_f32_16x16x32_bf16 v[90:93], v[202:205], v[102:105], v[90:93]
	v_mfma_f32_16x16x32_bf16 v[94:97], v[202:205], v[118:121], v[94:97]
	ds_read_b64_tr_b16 v[214:215], v180 offset:0
	ds_read_b64_tr_b16 v[216:217], v180 offset:4096
	ds_read_b64_tr_b16 v[218:219], v181 offset:0
	ds_read_b64_tr_b16 v[220:221], v181 offset:4096
	ds_read_b64_tr_b16 v[222:223], v180 offset:512
	ds_read_b64_tr_b16 v[224:225], v180 offset:4608
	ds_read_b64_tr_b16 v[226:227], v181 offset:512
	ds_read_b64_tr_b16 v[228:229], v181 offset:4608
	ds_read_b64_tr_b16 v[230:231], v180 offset:1024
	ds_read_b64_tr_b16 v[232:233], v180 offset:5120
	ds_read_b64_tr_b16 v[234:235], v181 offset:1024
	ds_read_b64_tr_b16 v[236:237], v181 offset:5120
	s_waitcnt lgkmcnt(12)
	v_mfma_f32_16x16x32_bf16 v[90:93], v[206:209], v[106:109], v[90:93]
	v_mfma_f32_16x16x32_bf16 v[94:97], v[206:209], v[122:125], v[94:97]
	v_mfma_f32_16x16x32_bf16 v[90:93], v[210:213], v[110:113], v[90:93]
	v_mfma_f32_16x16x32_bf16 v[94:97], v[210:213], v[126:129], v[94:97]
	s_waitcnt vmcnt(0) lgkmcnt(0)
	s_barrier
	s_cmp_ge_u32 s97, 130
	s_cbranch_scc1 .Lf16_se_N2
	s_add_i32 m0, s96, 0x8000
	s_nop 0
	global_load_lds_dwordx4 v170, s[2:3]
	s_add_i32 m0, s96, 0xa000
	s_nop 0
	global_load_lds_dwordx4 v172, s[2:3]
	s_add_i32 m0, s96, 0xc000
	s_nop 0
	global_load_lds_dwordx4 v171, s[2:3]
	s_add_i32 m0, s96, 0xe000
	s_nop 0
	global_load_lds_dwordx4 v173, s[2:3]
	s_add_u32 s2, s2, 0x4000
	s_addc_u32 s3, s3, 0
; #define SBAR() __builtin_amdgcn_sched_barrier(0)
; template <int D0> __device__ __forceinline__ void pv_rd(s16x4 (&r)[8], int vb) {
;   r[0] = tr_read<v_rd_off(D0, 0, 0)>(vb); r[1] = tr_read<v_rd_off(D0, 0, 1)>(vb); r[2] = tr_read<v_rd_off(D0, 1, 0)>(vb); r[3] = tr_read<v_rd_off(D0, 1, 1)>(vb);
;   r[4] = tr_read<v_rd_off(D0, 2, 0)>(vb); r[5] = tr_read<v_rd_off(D0, 2, 1)>(vb); r[6] = tr_read<v_rd_off(D0, 3, 0)>(vb); r[7] = tr_read<v_rd_off(D0, 3, 1)>(vb);
; }
; __device__ __forceinline__ void pv_mm(f32x16& od, const s16x4 (&r)[8], bf16x8 pa0, bf16x8 pa1, bf16x8 pa2, bf16x8 pa3) {
;     ...
;   od = __builtin_amdgcn_mfma_f32_32x32x16_bf16(pa0, PK(r[0], r[1]), od, 0, 0, 0);
;   od = __builtin_amdgcn_mfma_f32_32x32x16_bf16(pa1, PK(r[2], r[3]), od, 0, 0, 0);
;   od = __builtin_amdgcn_mfma_f32_32x32x16_bf16(pa2, PK(r[4], r[5]), od, 0, 0, 0);
;   od = __builtin_amdgcn_mfma_f32_32x32x16_bf16(pa3, PK(r[6], r[7]), od, 0, 0, 0);
;     ...
; }
; __device__ __forceinline__ void pv_d0(f32x16* o, int vb, bf16x8 pa0, bf16x8 pa1, bf16x8 pa2, bf16x8 pa3) {
;   s16x4 ra[8], rb[8];
;   pv_rd<0>(ra, vb); pv_rd<1>(rb, vb);
;   asm volatile("s_waitcnt lgkmcnt(8)" ::: "memory"); SBAR(); pv_mm(o[0], ra, pa0, pa1, pa2, pa3); pv_rd<2>(ra, vb);
;   asm volatile("s_waitcnt lgkmcnt(8)" ::: "memory"); SBAR(); pv_mm(o[1], rb, pa0, pa1, pa2, pa3); pv_rd<3>(rb, vb);
;   asm volatile("s_waitcnt lgkmcnt(8)" ::: "memory"); SBAR(); pv_mm(o[2], ra, pa0, pa1, pa2, pa3);
;   asm volatile("s_waitcnt lgkmcnt(0)" ::: "memory"); SBAR(); pv_mm(o[3], rb, pa0, pa1, pa2, pa3);
; }
.Lf16_se_N2:
	s_waitcnt lgkmcnt(8)
	v_mfma_f32_16x16x32_bf16 v[2:5], v[214:217], v[130:133], v[2:5]
	v_mfma_f32_16x16x32_bf16 v[6:9], v[214:217], v[138:141], v[6:9]
	v_exp_f32_e32 v66, v66
	v_mfma_f32_16x16x32_bf16 v[10:13], v[218:221], v[130:133], v[10:13]
	v_mfma_f32_16x16x32_bf16 v[14:17], v[218:221], v[138:141], v[14:17]
	v_exp_f32_e32 v67, v67
	ds_read_b64_tr_b16 v[238:239], v180 offset:1536
	ds_read_b64_tr_b16 v[240:241], v180 offset:5632
	ds_read_b64_tr_b16 v[242:243], v181 offset:1536
	ds_read_b64_tr_b16 v[244:245], v181 offset:5632
	s_waitcnt lgkmcnt(8)
	v_mfma_f32_16x16x32_bf16 v[18:21], v[222:225], v[130:133], v[18:21]
	v_mfma_f32_16x16x32_bf16 v[22:25], v[222:225], v[138:141], v[22:25]
	v_exp_f32_e32 v68, v68
	v_mfma_f32_16x16x32_bf16 v[26:29], v[226:229], v[130:133], v[26:29]
	v_mfma_f32_16x16x32_bf16 v[30:33], v[226:229], v[138:141], v[30:33]
	v_exp_f32_e32 v69, v69
	v_mfma_f32_16x16x32_bf16 v[246:249], v[194:197], v[130:133], v[246:249]
	ds_read_b64_tr_b16 v[214:215], v180 offset:8192
	ds_read_b64_tr_b16 v[216:217], v180 offset:12288
	ds_read_b64_tr_b16 v[218:219], v181 offset:8192
	ds_read_b64_tr_b16 v[220:221], v181 offset:12288
	s_waitcnt lgkmcnt(8)
	v_mfma_f32_16x16x32_bf16 v[34:37], v[230:233], v[130:133], v[34:37]
	v_mfma_f32_16x16x32_bf16 v[38:41], v[230:233], v[138:141], v[38:41]
	v_exp_f32_e32 v70, v70
	v_mfma_f32_16x16x32_bf16 v[42:45], v[234:237], v[130:133], v[42:45]
	v_mfma_f32_16x16x32_bf16 v[46:49], v[234:237], v[138:141], v[46:49]
	v_exp_f32_e32 v71, v71
	ds_read_b64_tr_b16 v[222:223], v180 offset:8704
	ds_read_b64_tr_b16 v[224:225], v180 offset:12800
	ds_read_b64_tr_b16 v[226:227], v181 offset:8704
	ds_read_b64_tr_b16 v[228:229], v181 offset:12800
	s_waitcnt lgkmcnt(8)
	v_mfma_f32_16x16x32_bf16 v[50:53], v[238:241], v[130:133], v[50:53]
	v_mfma_f32_16x16x32_bf16 v[54:57], v[238:241], v[138:141], v[54:57]
	v_exp_f32_e32 v72, v72
	v_mfma_f32_16x16x32_bf16 v[58:61], v[242:245], v[130:133], v[58:61]
	v_mfma_f32_16x16x32_bf16 v[62:65], v[242:245], v[138:141], v[62:65]
	v_exp_f32_e32 v73, v73
	v_mfma_f32_16x16x32_bf16 v[252:255], v[194:197], v[138:141], v[252:255]
	ds_read_b64_tr_b16 v[230:231], v180 offset:9216
	ds_read_b64_tr_b16 v[232:233], v180 offset:13312
	ds_read_b64_tr_b16 v[234:235], v181 offset:9216
	ds_read_b64_tr_b16 v[236:237], v181 offset:13312
	s_waitcnt lgkmcnt(8)
	v_mfma_f32_16x16x32_bf16 v[2:5], v[214:217], v[134:137], v[2:5]
	v_mfma_f32_16x16x32_bf16 v[6:9], v[214:217], v[142:145], v[6:9]
	v_exp_f32_e32 v74, v74
	v_mfma_f32_16x16x32_bf16 v[10:13], v[218:221], v[134:137], v[10:13]
	v_mfma_f32_16x16x32_bf16 v[14:17], v[218:221], v[142:145], v[14:17]
	v_exp_f32_e32 v75, v75
	ds_read_b64_tr_b16 v[238:239], v180 offset:9728
	ds_read_b64_tr_b16 v[240:241], v180 offset:13824
	ds_read_b64_tr_b16 v[242:243], v181 offset:9728
	ds_read_b64_tr_b16 v[244:245], v181 offset:13824
	s_waitcnt lgkmcnt(8)
	v_mfma_f32_16x16x32_bf16 v[18:21], v[222:225], v[134:137], v[18:21]
	v_mfma_f32_16x16x32_bf16 v[22:25], v[222:225], v[142:145], v[22:25]
	v_exp_f32_e32 v76, v76
	v_mfma_f32_16x16x32_bf16 v[26:29], v[226:229], v[134:137], v[26:29]
	v_mfma_f32_16x16x32_bf16 v[30:33], v[226:229], v[142:145], v[30:33]
	v_exp_f32_e32 v77, v77
	v_mfma_f32_16x16x32_bf16 v[246:249], v[194:197], v[134:137], v[246:249]
	s_waitcnt lgkmcnt(4)
	v_mfma_f32_16x16x32_bf16 v[34:37], v[230:233], v[134:137], v[34:37]
	v_mfma_f32_16x16x32_bf16 v[38:41], v[230:233], v[142:145], v[38:41]
	v_exp_f32_e32 v78, v78
	v_mfma_f32_16x16x32_bf16 v[42:45], v[234:237], v[134:137], v[42:45]
	v_mfma_f32_16x16x32_bf16 v[46:49], v[234:237], v[142:145], v[46:49]
	v_exp_f32_e32 v79, v79
	s_waitcnt lgkmcnt(0)
	v_mfma_f32_16x16x32_bf16 v[50:53], v[238:241], v[134:137], v[50:53]
	v_mfma_f32_16x16x32_bf16 v[54:57], v[238:241], v[142:145], v[54:57]
	v_exp_f32_e32 v80, v80
	v_mfma_f32_16x16x32_bf16 v[58:61], v[242:245], v[134:137], v[58:61]
	v_mfma_f32_16x16x32_bf16 v[62:65], v[242:245], v[142:145], v[62:65]
	v_exp_f32_e32 v81, v81
	v_mfma_f32_16x16x32_bf16 v[252:255], v[194:197], v[142:145], v[252:255]
	v_cvt_pk_bf16_f32 v130, v66, v67
	v_cvt_pk_bf16_f32 v131, v68, v69
	v_cvt_pk_bf16_f32 v132, v74, v75
	v_cvt_pk_bf16_f32 v133, v76, v77
	v_cvt_pk_bf16_f32 v138, v70, v71
	v_cvt_pk_bf16_f32 v139, v72, v73
	v_cvt_pk_bf16_f32 v140, v78, v79
	v_cvt_pk_bf16_f32 v141, v80, v81
	s_add_i32 s97, s97, 1
	s_cmp_lt_u32 s97, 132
	s_cbranch_scc0 .Lf16_done
; #define SBAR() __builtin_amdgcn_sched_barrier(0)
; #define ATT_SYNC(jn) do { ATT_WAIT_BAR(); if ((jn) < NT) ATT_DMA((jn), (jn) & 3); } while (0)
; __device__ __forceinline__ void qkt(f32x16& p0, f32x16& p1, const bf16_t* Ks, const bf16x8* qr, int r32, int hi) {
;   p0 = f32x16{}; p1 = f32x16{};
;   for (int d0 = 0; d0 < 8; ++d0) { int cb = (d0 * 16 + hi * 8) * 2;
;     bf16x8 b0 = *reinterpret_cast<const bf16x8*>((const char*)Ks + KSWZ(r32, cb));
;     bf16x8 b1 = *reinterpret_cast<const bf16x8*>((const char*)Ks + KSWZ(32 + r32, cb));
;     p0 = __builtin_amdgcn_mfma_f32_32x32x16_bf16(b0, qr[d0], p0, 0, 0, 0);
;     p1 = __builtin_amdgcn_mfma_f32_32x32x16_bf16(b1, qr[d0], p1, 0, 0, 0); }
; }
; __device__ __forceinline__ void attn_dma_body(const bf16_t* __restrict__ Qb, int ldq, int tpos0, const float* __restrict__ rope, const float* __restrict__ qgain, ...
;     ...
;   for (int j = 1; j + 1 < NT; j += 2) {
;     { SBAR(); qkt(pB0, pB1, (const bf16_t*)(lds + (j & 3) * SHM_SLOT), qr, r32, hi);
;       finishSM(pA0, pA1, alA, l_reg, pa0, pa1, pa2, pa3); s16x4 va[8]; pv_rd<0>(va, vb0 + ((j - 1) & 3) * (int)SHM_SLOT); SBAR();
;       if (!lead) ATT_SYNC(j + 2);
;       pv_d0_pre(o, vb0 + ((j - 1) & 3) * (int)SHM_SLOT, va, pa0, pa1, pa2, pa3); partialSM(pB0, pB1, m_reg, mnB, alB);
	ds_read_b128 v[146:149], v183 offset:0
	ds_read_b128 v[150:153], v184 offset:0
	ds_read_b128 v[154:157], v185 offset:0
	ds_read_b128 v[158:161], v186 offset:0
	ds_read_b128 v[198:201], v183 offset:4096
	ds_read_b128 v[202:205], v184 offset:4096
	ds_read_b128 v[206:209], v185 offset:4096
	ds_read_b128 v[210:213], v186 offset:4096
	s_waitcnt lgkmcnt(6)
	v_mfma_f32_16x16x32_bf16 v[66:69], v[146:149], v[98:101], 0
	v_exp_f32_e32 v82, v82
	v_mfma_f32_16x16x32_bf16 v[70:73], v[146:149], v[114:117], 0
	v_exp_f32_e32 v83, v83
	v_mfma_f32_16x16x32_bf16 v[66:69], v[150:153], v[102:105], v[66:69]
	v_exp_f32_e32 v84, v84
	v_mfma_f32_16x16x32_bf16 v[70:73], v[150:153], v[118:121], v[70:73]
	v_exp_f32_e32 v85, v85
	ds_read_b128 v[146:149], v183 offset:8192
	ds_read_b128 v[150:153], v184 offset:8192
	s_waitcnt lgkmcnt(6)
	v_mfma_f32_16x16x32_bf16 v[66:69], v[154:157], v[106:109], v[66:69]
	v_exp_f32_e32 v86, v86
	v_mfma_f32_16x16x32_bf16 v[70:73], v[154:157], v[122:125], v[70:73]
	v_exp_f32_e32 v87, v87
	v_mfma_f32_16x16x32_bf16 v[66:69], v[158:161], v[110:113], v[66:69]
	v_exp_f32_e32 v88, v88
	v_mfma_f32_16x16x32_bf16 v[70:73], v[158:161], v[126:129], v[70:73]
	v_exp_f32_e32 v89, v89
	ds_read_b128 v[154:157], v185 offset:8192
	ds_read_b128 v[158:161], v186 offset:8192
	s_waitcnt lgkmcnt(6)
	v_mfma_f32_16x16x32_bf16 v[74:77], v[198:201], v[98:101], 0
	v_exp_f32_e32 v90, v90
	v_mfma_f32_16x16x32_bf16 v[78:81], v[198:201], v[114:117], 0
	v_exp_f32_e32 v91, v91
	v_cvt_pk_bf16_f32 v134, v82, v83
	v_mfma_f32_16x16x32_bf16 v[74:77], v[202:205], v[102:105], v[74:77]
	v_exp_f32_e32 v92, v92
	v_cvt_pk_bf16_f32 v135, v84, v85
	v_mfma_f32_16x16x32_bf16 v[78:81], v[202:205], v[118:121], v[78:81]
	v_exp_f32_e32 v93, v93
	v_cvt_pk_bf16_f32 v142, v86, v87
	ds_read_b128 v[198:201], v183 offset:12288
	ds_read_b128 v[202:205], v184 offset:12288
	s_waitcnt lgkmcnt(6)
	v_mfma_f32_16x16x32_bf16 v[74:77], v[206:209], v[106:109], v[74:77]
	v_exp_f32_e32 v94, v94
	v_cvt_pk_bf16_f32 v143, v88, v89
	v_mfma_f32_16x16x32_bf16 v[78:81], v[206:209], v[122:125], v[78:81]
	v_exp_f32_e32 v95, v95
	v_mfma_f32_16x16x32_bf16 v[74:77], v[210:213], v[110:113], v[74:77]
	v_exp_f32_e32 v96, v96
	v_mfma_f32_16x16x32_bf16 v[78:81], v[210:213], v[126:129], v[78:81]
	v_exp_f32_e32 v97, v97
	ds_read_b128 v[206:209], v185 offset:12288
	ds_read_b128 v[210:213], v186 offset:12288
	s_waitcnt lgkmcnt(6)
	v_mfma_f32_16x16x32_bf16 v[82:85], v[146:149], v[98:101], 0
	v_mfma_f32_16x16x32_bf16 v[86:89], v[146:149], v[114:117], 0
	v_cvt_pk_bf16_f32 v136, v90, v91
	v_mfma_f32_16x16x32_bf16 v[82:85], v[150:153], v[102:105], v[82:85]
	v_cvt_pk_bf16_f32 v137, v92, v93
	v_mfma_f32_16x16x32_bf16 v[86:89], v[150:153], v[118:121], v[86:89]
	v_cvt_pk_bf16_f32 v144, v94, v95
	s_waitcnt lgkmcnt(4)
	v_mfma_f32_16x16x32_bf16 v[82:85], v[154:157], v[106:109], v[82:85]
	v_cvt_pk_bf16_f32 v145, v96, v97
	v_mfma_f32_16x16x32_bf16 v[86:89], v[154:157], v[122:125], v[86:89]
	v_mfma_f32_16x16x32_bf16 v[82:85], v[158:161], v[110:113], v[82:85]
	v_mfma_f32_16x16x32_bf16 v[86:89], v[158:161], v[126:129], v[86:89]
	s_waitcnt lgkmcnt(2)
	v_mfma_f32_16x16x32_bf16 v[90:93], v[198:201], v[98:101], 0
	v_mfma_f32_16x16x32_bf16 v[94:97], v[198:201], v[114:117], 0
	v_mfma_f32_16x16x32_bf16 v[90:93], v[202:205], v[102:105], v[90:93]
	v_mfma_f32_16x16x32_bf16 v[94:97], v[202:205], v[118:121], v[94:97]
	ds_read_b64_tr_b16 v[214:215], v180 offset:32768
	ds_read_b64_tr_b16 v[216:217], v180 offset:36864
	ds_read_b64_tr_b16 v[218:219], v181 offset:32768
	ds_read_b64_tr_b16 v[220:221], v181 offset:36864
	ds_read_b64_tr_b16 v[222:223], v180 offset:33280
	ds_read_b64_tr_b16 v[224:225], v180 offset:37376
	ds_read_b64_tr_b16 v[226:227], v181 offset:33280
	ds_read_b64_tr_b16 v[228:229], v181 offset:37376
	ds_read_b64_tr_b16 v[230:231], v180 offset:33792
	ds_read_b64_tr_b16 v[232:233], v180 offset:37888
	ds_read_b64_tr_b16 v[234:235], v181 offset:33792
	ds_read_b64_tr_b16 v[236:237], v181 offset:37888
	s_waitcnt lgkmcnt(12)
	v_mfma_f32_16x16x32_bf16 v[90:93], v[206:209], v[106:109], v[90:93]
	v_mfma_f32_16x16x32_bf16 v[94:97], v[206:209], v[122:125], v[94:97]
	v_mfma_f32_16x16x32_bf16 v[90:93], v[210:213], v[110:113], v[90:93]
	v_mfma_f32_16x16x32_bf16 v[94:97], v[210:213], v[126:129], v[94:97]
	s_waitcnt vmcnt(0) lgkmcnt(0)
	s_barrier
	s_cmp_ge_u32 s97, 130
	s_cbranch_scc1 .Lf16_se_N3
	s_add_i32 m0, s96, 0x10000
	s_nop 0
	global_load_lds_dwordx4 v170, s[2:3]
	s_add_i32 m0, s96, 0x12000
	s_nop 0
	global_load_lds_dwordx4 v172, s[2:3]
	s_add_i32 m0, s96, 0x14000
	s_nop 0
	global_load_lds_dwordx4 v171, s[2:3]
	s_add_i32 m0, s96, 0x16000
	s_nop 0
	global_load_lds_dwordx4 v173, s[2:3]
	s_add_u32 s2, s2, 0x4000
	s_addc_u32 s3, s3, 0
; #define SBAR() __builtin_amdgcn_sched_barrier(0)
; template <int D0> __device__ __forceinline__ void pv_rd(s16x4 (&r)[8], int vb) {
;   r[0] = tr_read<v_rd_off(D0, 0, 0)>(vb); r[1] = tr_read<v_rd_off(D0, 0, 1)>(vb); r[2] = tr_read<v_rd_off(D0, 1, 0)>(vb); r[3] = tr_read<v_rd_off(D0, 1, 1)>(vb);
;   r[4] = tr_read<v_rd_off(D0, 2, 0)>(vb); r[5] = tr_read<v_rd_off(D0, 2, 1)>(vb); r[6] = tr_read<v_rd_off(D0, 3, 0)>(vb); r[7] = tr_read<v_rd_off(D0, 3, 1)>(vb);
; }
; __device__ __forceinline__ void pv_mm(f32x16& od, const s16x4 (&r)[8], bf16x8 pa0, bf16x8 pa1, bf16x8 pa2, bf16x8 pa3) {
;     ...
;   od = __builtin_amdgcn_mfma_f32_32x32x16_bf16(pa0, PK(r[0], r[1]), od, 0, 0, 0);
;   od = __builtin_amdgcn_mfma_f32_32x32x16_bf16(pa1, PK(r[2], r[3]), od, 0, 0, 0);
;   od = __builtin_amdgcn_mfma_f32_32x32x16_bf16(pa2, PK(r[4], r[5]), od, 0, 0, 0);
;   od = __builtin_amdgcn_mfma_f32_32x32x16_bf16(pa3, PK(r[6], r[7]), od, 0, 0, 0);
;     ...
; }
; __device__ __forceinline__ void pv_d0(f32x16* o, int vb, bf16x8 pa0, bf16x8 pa1, bf16x8 pa2, bf16x8 pa3) {
;   s16x4 ra[8], rb[8];
;   pv_rd<0>(ra, vb); pv_rd<1>(rb, vb);
;   asm volatile("s_waitcnt lgkmcnt(8)" ::: "memory"); SBAR(); pv_mm(o[0], ra, pa0, pa1, pa2, pa3); pv_rd<2>(ra, vb);
;   asm volatile("s_waitcnt lgkmcnt(8)" ::: "memory"); SBAR(); pv_mm(o[1], rb, pa0, pa1, pa2, pa3); pv_rd<3>(rb, vb);
;   asm volatile("s_waitcnt lgkmcnt(8)" ::: "memory"); SBAR(); pv_mm(o[2], ra, pa0, pa1, pa2, pa3);
;   asm volatile("s_waitcnt lgkmcnt(0)" ::: "memory"); SBAR(); pv_mm(o[3], rb, pa0, pa1, pa2, pa3);
; }
.Lf16_se_N3:
	s_waitcnt lgkmcnt(8)
	v_mfma_f32_16x16x32_bf16 v[2:5], v[214:217], v[130:133], v[2:5]
	v_mfma_f32_16x16x32_bf16 v[6:9], v[214:217], v[138:141], v[6:9]
	v_exp_f32_e32 v66, v66
	v_mfma_f32_16x16x32_bf16 v[10:13], v[218:221], v[130:133], v[10:13]
	v_mfma_f32_16x16x32_bf16 v[14:17], v[218:221], v[138:141], v[14:17]
	v_exp_f32_e32 v67, v67
	ds_read_b64_tr_b16 v[238:239], v180 offset:34304
	ds_read_b64_tr_b16 v[240:241], v180 offset:38400
	ds_read_b64_tr_b16 v[242:243], v181 offset:34304
	ds_read_b64_tr_b16 v[244:245], v181 offset:38400
	s_waitcnt lgkmcnt(8)
	v_mfma_f32_16x16x32_bf16 v[18:21], v[222:225], v[130:133], v[18:21]
	v_mfma_f32_16x16x32_bf16 v[22:25], v[222:225], v[138:141], v[22:25]
	v_exp_f32_e32 v68, v68
	v_mfma_f32_16x16x32_bf16 v[26:29], v[226:229], v[130:133], v[26:29]
	v_mfma_f32_16x16x32_bf16 v[30:33], v[226:229], v[138:141], v[30:33]
	v_exp_f32_e32 v69, v69
	v_mfma_f32_16x16x32_bf16 v[246:249], v[194:197], v[130:133], v[246:249]
	ds_read_b64_tr_b16 v[214:215], v180 offset:40960
	ds_read_b64_tr_b16 v[216:217], v180 offset:45056
	ds_read_b64_tr_b16 v[218:219], v181 offset:40960
	ds_read_b64_tr_b16 v[220:221], v181 offset:45056
	s_waitcnt lgkmcnt(8)
	v_mfma_f32_16x16x32_bf16 v[34:37], v[230:233], v[130:133], v[34:37]
	v_mfma_f32_16x16x32_bf16 v[38:41], v[230:233], v[138:141], v[38:41]
	v_exp_f32_e32 v70, v70
	v_mfma_f32_16x16x32_bf16 v[42:45], v[234:237], v[130:133], v[42:45]
	v_mfma_f32_16x16x32_bf16 v[46:49], v[234:237], v[138:141], v[46:49]
	v_exp_f32_e32 v71, v71
	ds_read_b64_tr_b16 v[222:223], v180 offset:41472
	ds_read_b64_tr_b16 v[224:225], v180 offset:45568
	ds_read_b64_tr_b16 v[226:227], v181 offset:41472
	ds_read_b64_tr_b16 v[228:229], v181 offset:45568
	s_waitcnt lgkmcnt(8)
	v_mfma_f32_16x16x32_bf16 v[50:53], v[238:241], v[130:133], v[50:53]
	v_mfma_f32_16x16x32_bf16 v[54:57], v[238:241], v[138:141], v[54:57]
	v_exp_f32_e32 v72, v72
	v_mfma_f32_16x16x32_bf16 v[58:61], v[242:245], v[130:133], v[58:61]
	v_mfma_f32_16x16x32_bf16 v[62:65], v[242:245], v[138:141], v[62:65]
	v_exp_f32_e32 v73, v73
	v_mfma_f32_16x16x32_bf16 v[252:255], v[194:197], v[138:141], v[252:255]
	ds_read_b64_tr_b16 v[230:231], v180 offset:41984
	ds_read_b64_tr_b16 v[232:233], v180 offset:46080
	ds_read_b64_tr_b16 v[234:235], v181 offset:41984
	ds_read_b64_tr_b16 v[236:237], v181 offset:46080
	s_waitcnt lgkmcnt(8)
	v_mfma_f32_16x16x32_bf16 v[2:5], v[214:217], v[134:137], v[2:5]
	v_mfma_f32_16x16x32_bf16 v[6:9], v[214:217], v[142:145], v[6:9]
	v_exp_f32_e32 v74, v74
	v_mfma_f32_16x16x32_bf16 v[10:13], v[218:221], v[134:137], v[10:13]
	v_mfma_f32_16x16x32_bf16 v[14:17], v[218:221], v[142:145], v[14:17]
	v_exp_f32_e32 v75, v75
	ds_read_b64_tr_b16 v[238:239], v180 offset:42496
	ds_read_b64_tr_b16 v[240:241], v180 offset:46592
	ds_read_b64_tr_b16 v[242:243], v181 offset:42496
	ds_read_b64_tr_b16 v[244:245], v181 offset:46592
	s_waitcnt lgkmcnt(8)
	v_mfma_f32_16x16x32_bf16 v[18:21], v[222:225], v[134:137], v[18:21]
	v_mfma_f32_16x16x32_bf16 v[22:25], v[222:225], v[142:145], v[22:25]
	v_exp_f32_e32 v76, v76
	v_mfma_f32_16x16x32_bf16 v[26:29], v[226:229], v[134:137], v[26:29]
	v_mfma_f32_16x16x32_bf16 v[30:33], v[226:229], v[142:145], v[30:33]
	v_exp_f32_e32 v77, v77
	v_mfma_f32_16x16x32_bf16 v[246:249], v[194:197], v[134:137], v[246:249]
	s_waitcnt lgkmcnt(4)
	v_mfma_f32_16x16x32_bf16 v[34:37], v[230:233], v[134:137], v[34:37]
	v_mfma_f32_16x16x32_bf16 v[38:41], v[230:233], v[142:145], v[38:41]
	v_exp_f32_e32 v78, v78
	v_mfma_f32_16x16x32_bf16 v[42:45], v[234:237], v[134:137], v[42:45]
	v_mfma_f32_16x16x32_bf16 v[46:49], v[234:237], v[142:145], v[46:49]
	v_exp_f32_e32 v79, v79
	s_waitcnt lgkmcnt(0)
	v_mfma_f32_16x16x32_bf16 v[50:53], v[238:241], v[134:137], v[50:53]
	v_mfma_f32_16x16x32_bf16 v[54:57], v[238:241], v[142:145], v[54:57]
	v_exp_f32_e32 v80, v80
	v_mfma_f32_16x16x32_bf16 v[58:61], v[242:245], v[134:137], v[58:61]
	v_mfma_f32_16x16x32_bf16 v[62:65], v[242:245], v[142:145], v[62:65]
	v_exp_f32_e32 v81, v81
	v_mfma_f32_16x16x32_bf16 v[252:255], v[194:197], v[142:145], v[252:255]
	v_cvt_pk_bf16_f32 v130, v66, v67
	v_cvt_pk_bf16_f32 v131, v68, v69
	v_cvt_pk_bf16_f32 v132, v74, v75
	v_cvt_pk_bf16_f32 v133, v76, v77
	v_cvt_pk_bf16_f32 v138, v70, v71
	v_cvt_pk_bf16_f32 v139, v72, v73
	v_cvt_pk_bf16_f32 v140, v78, v79
	v_cvt_pk_bf16_f32 v141, v80, v81
	s_add_i32 s97, s97, 1
	s_branch .Lf16_N_loop
	.p2align 6
; #define SBAR() __builtin_amdgcn_sched_barrier(0)
; __device__ __forceinline__ void qkt(f32x16& p0, f32x16& p1, const bf16_t* Ks, const bf16x8* qr, int r32, int hi) {
;   p0 = f32x16{}; p1 = f32x16{};
;   for (int d0 = 0; d0 < 8; ++d0) { int cb = (d0 * 16 + hi * 8) * 2;
;     bf16x8 b0 = *reinterpret_cast<const bf16x8*>((const char*)Ks + KSWZ(r32, cb));
;     bf16x8 b1 = *reinterpret_cast<const bf16x8*>((const char*)Ks + KSWZ(32 + r32, cb));
;     p0 = __builtin_amdgcn_mfma_f32_32x32x16_bf16(b0, qr[d0], p0, 0, 0, 0);
;     p1 = __builtin_amdgcn_mfma_f32_32x32x16_bf16(b1, qr[d0], p1, 0, 0, 0); }
; }
; template <int D0> __device__ __forceinline__ void pv_rd(s16x4 (&r)[8], int vb) {
;   r[0] = tr_read<v_rd_off(D0, 0, 0)>(vb); r[1] = tr_read<v_rd_off(D0, 0, 1)>(vb); r[2] = tr_read<v_rd_off(D0, 1, 0)>(vb); r[3] = tr_read<v_rd_off(D0, 1, 1)>(vb);
;   r[4] = tr_read<v_rd_off(D0, 2, 0)>(vb); r[5] = tr_read<v_rd_off(D0, 2, 1)>(vb); r[6] = tr_read<v_rd_off(D0, 3, 0)>(vb); r[7] = tr_read<v_rd_off(D0, 3, 1)>(vb);
; }
; __device__ __forceinline__ void pv_mm(f32x16& od, const s16x4 (&r)[8], bf16x8 pa0, bf16x8 pa1, bf16x8 pa2, bf16x8 pa3) {
;     ...
;   od = __builtin_amdgcn_mfma_f32_32x32x16_bf16(pa0, PK(r[0], r[1]), od, 0, 0, 0);
;   od = __builtin_amdgcn_mfma_f32_32x32x16_bf16(pa1, PK(r[2], r[3]), od, 0, 0, 0);
;   od = __builtin_amdgcn_mfma_f32_32x32x16_bf16(pa2, PK(r[4], r[5]), od, 0, 0, 0);
;   od = __builtin_amdgcn_mfma_f32_32x32x16_bf16(pa3, PK(r[6], r[7]), od, 0, 0, 0);
;     ...
; }
; __device__ __forceinline__ void pv_d0(f32x16* o, int vb, bf16x8 pa0, bf16x8 pa1, bf16x8 pa2, bf16x8 pa3) {
;   s16x4 ra[8], rb[8];
;   pv_rd<0>(ra, vb); pv_rd<1>(rb, vb);
;   asm volatile("s_waitcnt lgkmcnt(8)" ::: "memory"); SBAR(); pv_mm(o[0], ra, pa0, pa1, pa2, pa3); pv_rd<2>(ra, vb);
;   asm volatile("s_waitcnt lgkmcnt(8)" ::: "memory"); SBAR(); pv_mm(o[1], rb, pa0, pa1, pa2, pa3); pv_rd<3>(rb, vb);
;   asm volatile("s_waitcnt lgkmcnt(8)" ::: "memory"); SBAR(); pv_mm(o[2], ra, pa0, pa1, pa2, pa3);
;   asm volatile("s_waitcnt lgkmcnt(0)" ::: "memory"); SBAR(); pv_mm(o[3], rb, pa0, pa1, pa2, pa3);
; }
.Lf16_L_loop:
	ds_read_b128 v[146:149], v183 offset:32768
	ds_read_b128 v[150:153], v184 offset:32768
	ds_read_b128 v[154:157], v185 offset:32768
	ds_read_b128 v[158:161], v186 offset:32768
	ds_read_b128 v[198:201], v183 offset:36864
	ds_read_b128 v[202:205], v184 offset:36864
	ds_read_b128 v[206:209], v185 offset:36864
	ds_read_b128 v[210:213], v186 offset:36864
	s_waitcnt lgkmcnt(6)
	v_mfma_f32_16x16x32_bf16 v[66:69], v[146:149], v[98:101], 0
	v_exp_f32_e32 v82, v82
	v_mfma_f32_16x16x32_bf16 v[70:73], v[146:149], v[114:117], 0
	v_exp_f32_e32 v83, v83
	v_mfma_f32_16x16x32_bf16 v[66:69], v[150:153], v[102:105], v[66:69]
	v_exp_f32_e32 v84, v84
	v_mfma_f32_16x16x32_bf16 v[70:73], v[150:153], v[118:121], v[70:73]
	v_exp_f32_e32 v85, v85
	ds_read_b128 v[146:149], v183 offset:40960
	ds_read_b128 v[150:153], v184 offset:40960
	s_waitcnt lgkmcnt(6)
	v_mfma_f32_16x16x32_bf16 v[66:69], v[154:157], v[106:109], v[66:69]
	v_exp_f32_e32 v86, v86
	v_mfma_f32_16x16x32_bf16 v[70:73], v[154:157], v[122:125], v[70:73]
	v_exp_f32_e32 v87, v87
	v_mfma_f32_16x16x32_bf16 v[66:69], v[158:161], v[110:113], v[66:69]
	v_exp_f32_e32 v88, v88
	v_mfma_f32_16x16x32_bf16 v[70:73], v[158:161], v[126:129], v[70:73]
	v_exp_f32_e32 v89, v89
	ds_read_b128 v[154:157], v185 offset:40960
	ds_read_b128 v[158:161], v186 offset:40960
	s_waitcnt lgkmcnt(6)
	v_mfma_f32_16x16x32_bf16 v[74:77], v[198:201], v[98:101], 0
	v_exp_f32_e32 v90, v90
	v_mfma_f32_16x16x32_bf16 v[78:81], v[198:201], v[114:117], 0
	v_exp_f32_e32 v91, v91
	v_cvt_pk_bf16_f32 v134, v82, v83
	v_mfma_f32_16x16x32_bf16 v[74:77], v[202:205], v[102:105], v[74:77]
	v_exp_f32_e32 v92, v92
	v_cvt_pk_bf16_f32 v135, v84, v85
	v_mfma_f32_16x16x32_bf16 v[78:81], v[202:205], v[118:121], v[78:81]
	v_exp_f32_e32 v93, v93
	v_cvt_pk_bf16_f32 v142, v86, v87
	ds_read_b128 v[198:201], v183 offset:45056
	ds_read_b128 v[202:205], v184 offset:45056
	s_waitcnt lgkmcnt(6)
	v_mfma_f32_16x16x32_bf16 v[74:77], v[206:209], v[106:109], v[74:77]
	v_exp_f32_e32 v94, v94
	v_cvt_pk_bf16_f32 v143, v88, v89
	v_mfma_f32_16x16x32_bf16 v[78:81], v[206:209], v[122:125], v[78:81]
	v_exp_f32_e32 v95, v95
	v_mfma_f32_16x16x32_bf16 v[74:77], v[210:213], v[110:113], v[74:77]
	v_exp_f32_e32 v96, v96
	v_mfma_f32_16x16x32_bf16 v[78:81], v[210:213], v[126:129], v[78:81]
	v_exp_f32_e32 v97, v97
	ds_read_b128 v[206:209], v185 offset:45056
	ds_read_b128 v[210:213], v186 offset:45056
	s_waitcnt lgkmcnt(6)
	v_mfma_f32_16x16x32_bf16 v[82:85], v[146:149], v[98:101], 0
	v_mfma_f32_16x16x32_bf16 v[86:89], v[146:149], v[114:117], 0
	v_cvt_pk_bf16_f32 v136, v90, v91
	v_mfma_f32_16x16x32_bf16 v[82:85], v[150:153], v[102:105], v[82:85]
	v_cvt_pk_bf16_f32 v137, v92, v93
	v_mfma_f32_16x16x32_bf16 v[86:89], v[150:153], v[118:121], v[86:89]
	v_cvt_pk_bf16_f32 v144, v94, v95
	s_waitcnt lgkmcnt(4)
	v_mfma_f32_16x16x32_bf16 v[82:85], v[154:157], v[106:109], v[82:85]
	v_cvt_pk_bf16_f32 v145, v96, v97
	v_mfma_f32_16x16x32_bf16 v[86:89], v[154:157], v[122:125], v[86:89]
	v_mfma_f32_16x16x32_bf16 v[82:85], v[158:161], v[110:113], v[82:85]
	v_mfma_f32_16x16x32_bf16 v[86:89], v[158:161], v[126:129], v[86:89]
	s_waitcnt lgkmcnt(2)
	v_mfma_f32_16x16x32_bf16 v[90:93], v[198:201], v[98:101], 0
	v_mfma_f32_16x16x32_bf16 v[94:97], v[198:201], v[114:117], 0
	v_mfma_f32_16x16x32_bf16 v[90:93], v[202:205], v[102:105], v[90:93]
	v_mfma_f32_16x16x32_bf16 v[94:97], v[202:205], v[118:121], v[94:97]
	ds_read_b64_tr_b16 v[214:215], v191 offset:0
	ds_read_b64_tr_b16 v[216:217], v191 offset:4096
	ds_read_b64_tr_b16 v[218:219], v192 offset:0
	ds_read_b64_tr_b16 v[220:221], v192 offset:4096
	ds_read_b64_tr_b16 v[222:223], v191 offset:512
	ds_read_b64_tr_b16 v[224:225], v191 offset:4608
	ds_read_b64_tr_b16 v[226:227], v192 offset:512
	ds_read_b64_tr_b16 v[228:229], v192 offset:4608
	ds_read_b64_tr_b16 v[230:231], v191 offset:1024
	ds_read_b64_tr_b16 v[232:233], v191 offset:5120
	ds_read_b64_tr_b16 v[234:235], v192 offset:1024
	ds_read_b64_tr_b16 v[236:237], v192 offset:5120
	s_waitcnt lgkmcnt(12)
	v_mfma_f32_16x16x32_bf16 v[90:93], v[206:209], v[106:109], v[90:93]
	v_mfma_f32_16x16x32_bf16 v[94:97], v[206:209], v[122:125], v[94:97]
	v_mfma_f32_16x16x32_bf16 v[90:93], v[210:213], v[110:113], v[90:93]
	v_mfma_f32_16x16x32_bf16 v[94:97], v[210:213], v[126:129], v[94:97]
	s_waitcnt lgkmcnt(8)
	v_mfma_f32_16x16x32_bf16 v[2:5], v[214:217], v[130:133], v[2:5]
	v_mfma_f32_16x16x32_bf16 v[6:9], v[214:217], v[138:141], v[6:9]
	v_exp_f32_e32 v66, v66
	v_mfma_f32_16x16x32_bf16 v[10:13], v[218:221], v[130:133], v[10:13]
	v_mfma_f32_16x16x32_bf16 v[14:17], v[218:221], v[138:141], v[14:17]
	v_exp_f32_e32 v67, v67
	ds_read_b64_tr_b16 v[238:239], v191 offset:1536
	ds_read_b64_tr_b16 v[240:241], v191 offset:5632
	ds_read_b64_tr_b16 v[242:243], v192 offset:1536
	ds_read_b64_tr_b16 v[244:245], v192 offset:5632
	s_waitcnt lgkmcnt(8)
	v_mfma_f32_16x16x32_bf16 v[18:21], v[222:225], v[130:133], v[18:21]
	v_mfma_f32_16x16x32_bf16 v[22:25], v[222:225], v[138:141], v[22:25]
	v_exp_f32_e32 v68, v68
	v_mfma_f32_16x16x32_bf16 v[26:29], v[226:229], v[130:133], v[26:29]
	v_mfma_f32_16x16x32_bf16 v[30:33], v[226:229], v[138:141], v[30:33]
	v_exp_f32_e32 v69, v69
	v_mfma_f32_16x16x32_bf16 v[246:249], v[194:197], v[130:133], v[246:249]
	ds_read_b64_tr_b16 v[214:215], v191 offset:8192
	ds_read_b64_tr_b16 v[216:217], v191 offset:12288
	ds_read_b64_tr_b16 v[218:219], v192 offset:8192
	ds_read_b64_tr_b16 v[220:221], v192 offset:12288
	s_waitcnt lgkmcnt(8)
; #define SBAR() __builtin_amdgcn_sched_barrier(0)
; #define RESC(a) do { if (__any((a) < 1.f)) { if (hi == 0) al_l[r32] = (a); asm volatile("s_waitcnt lgkmcnt(0)" ::: "memory"); \
;     for (int d = 0; d < 4; ++d) for (int r = 0; r < 16; ++r) o[d][r] *= al_l[crow(r, hi)]; } } while (0)
; #define RESC(a) do { if (__any((a) < 1.f)) { if (hi == 0) al_l[r32] = (a); asm volatile("s_waitcnt lgkmcnt(0)" ::: "memory"); \
;     for (int d = 0; d < 4; ++d) for (int r = 0; r < 16; ++r) o[d][r] *= al_l[crow(r, hi)]; } } while (0)
; #define ATT_SYNC(jn) do { ATT_WAIT_BAR(); if ((jn) < NT) ATT_DMA((jn), (jn) & 3); } while (0)
; __device__ __forceinline__ void attn_dma_body(const bf16_t* __restrict__ Qb, int ldq, int tpos0, const float* __restrict__ rope, const float* __restrict__ qgain, ...
;     ...
;   for (int j = 1; j + 1 < NT; j += 2) {
;     { SBAR(); qkt(pB0, pB1, (const bf16_t*)(lds + (j & 3) * SHM_SLOT), qr, r32, hi);
;       finishSM(pA0, pA1, alA, l_reg, pa0, pa1, pa2, pa3); s16x4 va[8]; pv_rd<0>(va, vb0 + ((j - 1) & 3) * (int)SHM_SLOT); SBAR();
;       if (!lead) ATT_SYNC(j + 2);
;       pv_d0_pre(o, vb0 + ((j - 1) & 3) * (int)SHM_SLOT, va, pa0, pa1, pa2, pa3); partialSM(pB0, pB1, m_reg, mnB, alB);
;       if (lead) ATT_SYNC(j + 2);
;       RESC(alB); }
;     { SBAR(); qkt(pA0, pA1, (const bf16_t*)(lds + ((j + 1) & 3) * SHM_SLOT), qr, r32, hi);
;       finishSM(pB0, pB1, alB, l_reg, pa0, pa1, pa2, pa3); s16x4 va[8]; pv_rd<0>(va, vb0 + (j & 3) * (int)SHM_SLOT); SBAR();
;       if (!lead) ATT_SYNC(j + 3);
;       pv_d0_pre(o, vb0 + (j & 3) * (int)SHM_SLOT, va, pa0, pa1, pa2, pa3); partialSM(pA0, pA1, m_reg, mnA, alA);
;       if (lead) ATT_SYNC(j + 3);
;       RESC(alA); }
;   }
	v_mfma_f32_16x16x32_bf16 v[34:37], v[230:233], v[130:133], v[34:37]
	v_mfma_f32_16x16x32_bf16 v[38:41], v[230:233], v[138:141], v[38:41]
	v_exp_f32_e32 v70, v70
	v_mfma_f32_16x16x32_bf16 v[42:45], v[234:237], v[130:133], v[42:45]
	v_mfma_f32_16x16x32_bf16 v[46:49], v[234:237], v[138:141], v[46:49]
	v_exp_f32_e32 v71, v71
	ds_read_b64_tr_b16 v[222:223], v191 offset:8704
	ds_read_b64_tr_b16 v[224:225], v191 offset:12800
	ds_read_b64_tr_b16 v[226:227], v192 offset:8704
	ds_read_b64_tr_b16 v[228:229], v192 offset:12800
	s_waitcnt lgkmcnt(8)
	v_mfma_f32_16x16x32_bf16 v[50:53], v[238:241], v[130:133], v[50:53]
	v_mfma_f32_16x16x32_bf16 v[54:57], v[238:241], v[138:141], v[54:57]
	v_exp_f32_e32 v72, v72
	v_mfma_f32_16x16x32_bf16 v[58:61], v[242:245], v[130:133], v[58:61]
	v_mfma_f32_16x16x32_bf16 v[62:65], v[242:245], v[138:141], v[62:65]
	v_exp_f32_e32 v73, v73
	v_mfma_f32_16x16x32_bf16 v[252:255], v[194:197], v[138:141], v[252:255]
	ds_read_b64_tr_b16 v[230:231], v191 offset:9216
	ds_read_b64_tr_b16 v[232:233], v191 offset:13312
	ds_read_b64_tr_b16 v[234:235], v192 offset:9216
	ds_read_b64_tr_b16 v[236:237], v192 offset:13312
	s_waitcnt lgkmcnt(8)
	v_mfma_f32_16x16x32_bf16 v[2:5], v[214:217], v[134:137], v[2:5]
	v_mfma_f32_16x16x32_bf16 v[6:9], v[214:217], v[142:145], v[6:9]
	v_exp_f32_e32 v74, v74
	v_mfma_f32_16x16x32_bf16 v[10:13], v[218:221], v[134:137], v[10:13]
	v_mfma_f32_16x16x32_bf16 v[14:17], v[218:221], v[142:145], v[14:17]
	v_exp_f32_e32 v75, v75
	ds_read_b64_tr_b16 v[238:239], v191 offset:9728
	ds_read_b64_tr_b16 v[240:241], v191 offset:13824
	ds_read_b64_tr_b16 v[242:243], v192 offset:9728
	ds_read_b64_tr_b16 v[244:245], v192 offset:13824
	s_waitcnt lgkmcnt(8)
	v_mfma_f32_16x16x32_bf16 v[18:21], v[222:225], v[134:137], v[18:21]
	v_mfma_f32_16x16x32_bf16 v[22:25], v[222:225], v[142:145], v[22:25]
	v_exp_f32_e32 v76, v76
	v_mfma_f32_16x16x32_bf16 v[26:29], v[226:229], v[134:137], v[26:29]
	v_mfma_f32_16x16x32_bf16 v[30:33], v[226:229], v[142:145], v[30:33]
	v_exp_f32_e32 v77, v77
	v_mfma_f32_16x16x32_bf16 v[246:249], v[194:197], v[134:137], v[246:249]
	s_waitcnt lgkmcnt(4)
	v_mfma_f32_16x16x32_bf16 v[34:37], v[230:233], v[134:137], v[34:37]
	v_mfma_f32_16x16x32_bf16 v[38:41], v[230:233], v[142:145], v[38:41]
	v_exp_f32_e32 v78, v78
	v_mfma_f32_16x16x32_bf16 v[42:45], v[234:237], v[134:137], v[42:45]
	v_mfma_f32_16x16x32_bf16 v[46:49], v[234:237], v[142:145], v[46:49]
	v_exp_f32_e32 v79, v79
	s_waitcnt lgkmcnt(0)
	v_mfma_f32_16x16x32_bf16 v[50:53], v[238:241], v[134:137], v[50:53]
	v_mfma_f32_16x16x32_bf16 v[54:57], v[238:241], v[142:145], v[54:57]
	v_exp_f32_e32 v80, v80
	v_mfma_f32_16x16x32_bf16 v[58:61], v[242:245], v[134:137], v[58:61]
	v_mfma_f32_16x16x32_bf16 v[62:65], v[242:245], v[142:145], v[62:65]
	v_exp_f32_e32 v81, v81
	v_mfma_f32_16x16x32_bf16 v[252:255], v[194:197], v[142:145], v[252:255]
	s_waitcnt vmcnt(0) lgkmcnt(0)
	s_barrier
	s_cmp_ge_u32 s97, 130
	s_cbranch_scc1 .Lf16_se_L0
	s_add_i32 m0, s96, 0x18000
	s_nop 0
	global_load_lds_dwordx4 v170, s[2:3]
	s_add_i32 m0, s96, 0x1a000
	s_nop 0
	global_load_lds_dwordx4 v172, s[2:3]
	s_add_i32 m0, s96, 0x1c000
	s_nop 0
	global_load_lds_dwordx4 v171, s[2:3]
	s_add_i32 m0, s96, 0x1e000
	s_nop 0
	global_load_lds_dwordx4 v173, s[2:3]
	s_add_u32 s2, s2, 0x4000
	s_addc_u32 s3, s3, 0
.Lf16_se_L0:
	v_cvt_pk_bf16_f32 v130, v66, v67
	v_cvt_pk_bf16_f32 v131, v68, v69
	v_cvt_pk_bf16_f32 v132, v74, v75
	v_cvt_pk_bf16_f32 v133, v76, v77
	v_cvt_pk_bf16_f32 v138, v70, v71
	v_cvt_pk_bf16_f32 v139, v72, v73
	v_cvt_pk_bf16_f32 v140, v78, v79
	v_cvt_pk_bf16_f32 v141, v80, v81
	s_add_i32 s97, s97, 1
	ds_read_b128 v[146:149], v187 offset:0
	ds_read_b128 v[150:153], v188 offset:0
	ds_read_b128 v[154:157], v189 offset:0
	ds_read_b128 v[158:161], v190 offset:0
	ds_read_b128 v[198:201], v187 offset:4096
	ds_read_b128 v[202:205], v188 offset:4096
	ds_read_b128 v[206:209], v189 offset:4096
	ds_read_b128 v[210:213], v190 offset:4096
	s_waitcnt lgkmcnt(6)
	v_mfma_f32_16x16x32_bf16 v[66:69], v[146:149], v[98:101], 0
	v_exp_f32_e32 v82, v82
	v_mfma_f32_16x16x32_bf16 v[70:73], v[146:149], v[114:117], 0
	v_exp_f32_e32 v83, v83
	v_mfma_f32_16x16x32_bf16 v[66:69], v[150:153], v[102:105], v[66:69]
	v_exp_f32_e32 v84, v84
	v_mfma_f32_16x16x32_bf16 v[70:73], v[150:153], v[118:121], v[70:73]
	v_exp_f32_e32 v85, v85
	ds_read_b128 v[146:149], v187 offset:8192
	ds_read_b128 v[150:153], v188 offset:8192
	s_waitcnt lgkmcnt(6)
	v_mfma_f32_16x16x32_bf16 v[66:69], v[154:157], v[106:109], v[66:69]
	v_exp_f32_e32 v86, v86
	v_mfma_f32_16x16x32_bf16 v[70:73], v[154:157], v[122:125], v[70:73]
	v_exp_f32_e32 v87, v87
	v_mfma_f32_16x16x32_bf16 v[66:69], v[158:161], v[110:113], v[66:69]
	v_exp_f32_e32 v88, v88
	v_mfma_f32_16x16x32_bf16 v[70:73], v[158:161], v[126:129], v[70:73]
	v_exp_f32_e32 v89, v89
	ds_read_b128 v[154:157], v189 offset:8192
	ds_read_b128 v[158:161], v190 offset:8192
	s_waitcnt lgkmcnt(6)
	v_mfma_f32_16x16x32_bf16 v[74:77], v[198:201], v[98:101], 0
	v_exp_f32_e32 v90, v90
	v_mfma_f32_16x16x32_bf16 v[78:81], v[198:201], v[114:117], 0
	v_exp_f32_e32 v91, v91
	v_cvt_pk_bf16_f32 v134, v82, v83
	v_mfma_f32_16x16x32_bf16 v[74:77], v[202:205], v[102:105], v[74:77]
	v_exp_f32_e32 v92, v92
	v_cvt_pk_bf16_f32 v135, v84, v85
	v_mfma_f32_16x16x32_bf16 v[78:81], v[202:205], v[118:121], v[78:81]
	v_exp_f32_e32 v93, v93
	v_cvt_pk_bf16_f32 v142, v86, v87
	ds_read_b128 v[198:201], v187 offset:12288
	ds_read_b128 v[202:205], v188 offset:12288
	s_waitcnt lgkmcnt(6)
; #define SBAR() __builtin_amdgcn_sched_barrier(0)
; __device__ __forceinline__ void qkt(f32x16& p0, f32x16& p1, const bf16_t* Ks, const bf16x8* qr, int r32, int hi) {
;   p0 = f32x16{}; p1 = f32x16{};
;   for (int d0 = 0; d0 < 8; ++d0) { int cb = (d0 * 16 + hi * 8) * 2;
;     bf16x8 b0 = *reinterpret_cast<const bf16x8*>((const char*)Ks + KSWZ(r32, cb));
;     bf16x8 b1 = *reinterpret_cast<const bf16x8*>((const char*)Ks + KSWZ(32 + r32, cb));
;     p0 = __builtin_amdgcn_mfma_f32_32x32x16_bf16(b0, qr[d0], p0, 0, 0, 0);
;     p1 = __builtin_amdgcn_mfma_f32_32x32x16_bf16(b1, qr[d0], p1, 0, 0, 0); }
; }
; template <int D0> __device__ __forceinline__ void pv_rd(s16x4 (&r)[8], int vb) {
;   r[0] = tr_read<v_rd_off(D0, 0, 0)>(vb); r[1] = tr_read<v_rd_off(D0, 0, 1)>(vb); r[2] = tr_read<v_rd_off(D0, 1, 0)>(vb); r[3] = tr_read<v_rd_off(D0, 1, 1)>(vb);
;   r[4] = tr_read<v_rd_off(D0, 2, 0)>(vb); r[5] = tr_read<v_rd_off(D0, 2, 1)>(vb); r[6] = tr_read<v_rd_off(D0, 3, 0)>(vb); r[7] = tr_read<v_rd_off(D0, 3, 1)>(vb);
; }
; __device__ __forceinline__ void pv_mm(f32x16& od, const s16x4 (&r)[8], bf16x8 pa0, bf16x8 pa1, bf16x8 pa2, bf16x8 pa3) {
;     ...
;   od = __builtin_amdgcn_mfma_f32_32x32x16_bf16(pa0, PK(r[0], r[1]), od, 0, 0, 0);
;   od = __builtin_amdgcn_mfma_f32_32x32x16_bf16(pa1, PK(r[2], r[3]), od, 0, 0, 0);
;   od = __builtin_amdgcn_mfma_f32_32x32x16_bf16(pa2, PK(r[4], r[5]), od, 0, 0, 0);
;   od = __builtin_amdgcn_mfma_f32_32x32x16_bf16(pa3, PK(r[6], r[7]), od, 0, 0, 0);
;     ...
; }
; __device__ __forceinline__ void pv_d0(f32x16* o, int vb, bf16x8 pa0, bf16x8 pa1, bf16x8 pa2, bf16x8 pa3) {
;   s16x4 ra[8], rb[8];
;   pv_rd<0>(ra, vb); pv_rd<1>(rb, vb);
;   asm volatile("s_waitcnt lgkmcnt(8)" ::: "memory"); SBAR(); pv_mm(o[0], ra, pa0, pa1, pa2, pa3); pv_rd<2>(ra, vb);
;   asm volatile("s_waitcnt lgkmcnt(8)" ::: "memory"); SBAR(); pv_mm(o[1], rb, pa0, pa1, pa2, pa3); pv_rd<3>(rb, vb);
;   asm volatile("s_waitcnt lgkmcnt(8)" ::: "memory"); SBAR(); pv_mm(o[2], ra, pa0, pa1, pa2, pa3);
;   asm volatile("s_waitcnt lgkmcnt(0)" ::: "memory"); SBAR(); pv_mm(o[3], rb, pa0, pa1, pa2, pa3);
; }
	v_mfma_f32_16x16x32_bf16 v[74:77], v[206:209], v[106:109], v[74:77]
	v_exp_f32_e32 v94, v94
	v_cvt_pk_bf16_f32 v143, v88, v89
	v_mfma_f32_16x16x32_bf16 v[78:81], v[206:209], v[122:125], v[78:81]
	v_exp_f32_e32 v95, v95
	v_mfma_f32_16x16x32_bf16 v[74:77], v[210:213], v[110:113], v[74:77]
	v_exp_f32_e32 v96, v96
	v_mfma_f32_16x16x32_bf16 v[78:81], v[210:213], v[126:129], v[78:81]
	v_exp_f32_e32 v97, v97
	ds_read_b128 v[206:209], v189 offset:12288
	ds_read_b128 v[210:213], v190 offset:12288
	s_waitcnt lgkmcnt(6)
	v_mfma_f32_16x16x32_bf16 v[82:85], v[146:149], v[98:101], 0
	v_mfma_f32_16x16x32_bf16 v[86:89], v[146:149], v[114:117], 0
	v_cvt_pk_bf16_f32 v136, v90, v91
	v_mfma_f32_16x16x32_bf16 v[82:85], v[150:153], v[102:105], v[82:85]
	v_cvt_pk_bf16_f32 v137, v92, v93
	v_mfma_f32_16x16x32_bf16 v[86:89], v[150:153], v[118:121], v[86:89]
	v_cvt_pk_bf16_f32 v144, v94, v95
	s_waitcnt lgkmcnt(4)
	v_mfma_f32_16x16x32_bf16 v[82:85], v[154:157], v[106:109], v[82:85]
	v_cvt_pk_bf16_f32 v145, v96, v97
	v_mfma_f32_16x16x32_bf16 v[86:89], v[154:157], v[122:125], v[86:89]
	v_mfma_f32_16x16x32_bf16 v[82:85], v[158:161], v[110:113], v[82:85]
	v_mfma_f32_16x16x32_bf16 v[86:89], v[158:161], v[126:129], v[86:89]
	s_waitcnt lgkmcnt(2)
	v_mfma_f32_16x16x32_bf16 v[90:93], v[198:201], v[98:101], 0
	v_mfma_f32_16x16x32_bf16 v[94:97], v[198:201], v[114:117], 0
	v_mfma_f32_16x16x32_bf16 v[90:93], v[202:205], v[102:105], v[90:93]
	v_mfma_f32_16x16x32_bf16 v[94:97], v[202:205], v[118:121], v[94:97]
	ds_read_b64_tr_b16 v[214:215], v191 offset:32768
	ds_read_b64_tr_b16 v[216:217], v191 offset:36864
	ds_read_b64_tr_b16 v[218:219], v192 offset:32768
	ds_read_b64_tr_b16 v[220:221], v192 offset:36864
	ds_read_b64_tr_b16 v[222:223], v191 offset:33280
	ds_read_b64_tr_b16 v[224:225], v191 offset:37376
	ds_read_b64_tr_b16 v[226:227], v192 offset:33280
	ds_read_b64_tr_b16 v[228:229], v192 offset:37376
	ds_read_b64_tr_b16 v[230:231], v191 offset:33792
	ds_read_b64_tr_b16 v[232:233], v191 offset:37888
	ds_read_b64_tr_b16 v[234:235], v192 offset:33792
	ds_read_b64_tr_b16 v[236:237], v192 offset:37888
	s_waitcnt lgkmcnt(12)
	v_mfma_f32_16x16x32_bf16 v[90:93], v[206:209], v[106:109], v[90:93]
	v_mfma_f32_16x16x32_bf16 v[94:97], v[206:209], v[122:125], v[94:97]
	v_mfma_f32_16x16x32_bf16 v[90:93], v[210:213], v[110:113], v[90:93]
	v_mfma_f32_16x16x32_bf16 v[94:97], v[210:213], v[126:129], v[94:97]
	s_waitcnt lgkmcnt(8)
	v_mfma_f32_16x16x32_bf16 v[2:5], v[214:217], v[130:133], v[2:5]
	v_mfma_f32_16x16x32_bf16 v[6:9], v[214:217], v[138:141], v[6:9]
	v_exp_f32_e32 v66, v66
	v_mfma_f32_16x16x32_bf16 v[10:13], v[218:221], v[130:133], v[10:13]
	v_mfma_f32_16x16x32_bf16 v[14:17], v[218:221], v[138:141], v[14:17]
	v_exp_f32_e32 v67, v67
	ds_read_b64_tr_b16 v[238:239], v191 offset:34304
	ds_read_b64_tr_b16 v[240:241], v191 offset:38400
	ds_read_b64_tr_b16 v[242:243], v192 offset:34304
	ds_read_b64_tr_b16 v[244:245], v192 offset:38400
	s_waitcnt lgkmcnt(8)
	v_mfma_f32_16x16x32_bf16 v[18:21], v[222:225], v[130:133], v[18:21]
	v_mfma_f32_16x16x32_bf16 v[22:25], v[222:225], v[138:141], v[22:25]
	v_exp_f32_e32 v68, v68
	v_mfma_f32_16x16x32_bf16 v[26:29], v[226:229], v[130:133], v[26:29]
	v_mfma_f32_16x16x32_bf16 v[30:33], v[226:229], v[138:141], v[30:33]
	v_exp_f32_e32 v69, v69
	v_mfma_f32_16x16x32_bf16 v[246:249], v[194:197], v[130:133], v[246:249]
	ds_read_b64_tr_b16 v[214:215], v191 offset:40960
	ds_read_b64_tr_b16 v[216:217], v191 offset:45056
	ds_read_b64_tr_b16 v[218:219], v192 offset:40960
	ds_read_b64_tr_b16 v[220:221], v192 offset:45056
	s_waitcnt lgkmcnt(8)
	v_mfma_f32_16x16x32_bf16 v[34:37], v[230:233], v[130:133], v[34:37]
	v_mfma_f32_16x16x32_bf16 v[38:41], v[230:233], v[138:141], v[38:41]
	v_exp_f32_e32 v70, v70
	v_mfma_f32_16x16x32_bf16 v[42:45], v[234:237], v[130:133], v[42:45]
	v_mfma_f32_16x16x32_bf16 v[46:49], v[234:237], v[138:141], v[46:49]
	v_exp_f32_e32 v71, v71
	ds_read_b64_tr_b16 v[222:223], v191 offset:41472
	ds_read_b64_tr_b16 v[224:225], v191 offset:45568
	ds_read_b64_tr_b16 v[226:227], v192 offset:41472
	ds_read_b64_tr_b16 v[228:229], v192 offset:45568
	s_waitcnt lgkmcnt(8)
	v_mfma_f32_16x16x32_bf16 v[50:53], v[238:241], v[130:133], v[50:53]
	v_mfma_f32_16x16x32_bf16 v[54:57], v[238:241], v[138:141], v[54:57]
	v_exp_f32_e32 v72, v72
	v_mfma_f32_16x16x32_bf16 v[58:61], v[242:245], v[130:133], v[58:61]
	v_mfma_f32_16x16x32_bf16 v[62:65], v[242:245], v[138:141], v[62:65]
	v_exp_f32_e32 v73, v73
	v_mfma_f32_16x16x32_bf16 v[252:255], v[194:197], v[138:141], v[252:255]
	ds_read_b64_tr_b16 v[230:231], v191 offset:41984
	ds_read_b64_tr_b16 v[232:233], v191 offset:46080
	ds_read_b64_tr_b16 v[234:235], v192 offset:41984
	ds_read_b64_tr_b16 v[236:237], v192 offset:46080
	s_waitcnt lgkmcnt(8)
	v_mfma_f32_16x16x32_bf16 v[2:5], v[214:217], v[134:137], v[2:5]
	v_mfma_f32_16x16x32_bf16 v[6:9], v[214:217], v[142:145], v[6:9]
	v_exp_f32_e32 v74, v74
	v_mfma_f32_16x16x32_bf16 v[10:13], v[218:221], v[134:137], v[10:13]
	v_mfma_f32_16x16x32_bf16 v[14:17], v[218:221], v[142:145], v[14:17]
	v_exp_f32_e32 v75, v75
	ds_read_b64_tr_b16 v[238:239], v191 offset:42496
	ds_read_b64_tr_b16 v[240:241], v191 offset:46592
	ds_read_b64_tr_b16 v[242:243], v192 offset:42496
	ds_read_b64_tr_b16 v[244:245], v192 offset:46592
	s_waitcnt lgkmcnt(8)
	v_mfma_f32_16x16x32_bf16 v[18:21], v[222:225], v[134:137], v[18:21]
	v_mfma_f32_16x16x32_bf16 v[22:25], v[222:225], v[142:145], v[22:25]
	v_exp_f32_e32 v76, v76
	v_mfma_f32_16x16x32_bf16 v[26:29], v[226:229], v[134:137], v[26:29]
	v_mfma_f32_16x16x32_bf16 v[30:33], v[226:229], v[142:145], v[30:33]
	v_exp_f32_e32 v77, v77
	v_mfma_f32_16x16x32_bf16 v[246:249], v[194:197], v[134:137], v[246:249]
	s_waitcnt lgkmcnt(4)
	v_mfma_f32_16x16x32_bf16 v[34:37], v[230:233], v[134:137], v[34:37]
	v_mfma_f32_16x16x32_bf16 v[38:41], v[230:233], v[142:145], v[38:41]
	v_exp_f32_e32 v78, v78
	v_mfma_f32_16x16x32_bf16 v[42:45], v[234:237], v[134:137], v[42:45]
	v_mfma_f32_16x16x32_bf16 v[46:49], v[234:237], v[142:145], v[46:49]
	v_exp_f32_e32 v79, v79
	s_waitcnt lgkmcnt(0)
	v_mfma_f32_16x16x32_bf16 v[50:53], v[238:241], v[134:137], v[50:53]
	v_mfma_f32_16x16x32_bf16 v[54:57], v[238:241], v[142:145], v[54:57]
	v_exp_f32_e32 v80, v80
	v_mfma_f32_16x16x32_bf16 v[58:61], v[242:245], v[134:137], v[58:61]
	v_mfma_f32_16x16x32_bf16 v[62:65], v[242:245], v[142:145], v[62:65]
	v_exp_f32_e32 v81, v81
	v_mfma_f32_16x16x32_bf16 v[252:255], v[194:197], v[142:145], v[252:255]
	s_waitcnt vmcnt(0) lgkmcnt(0)
	s_barrier
	s_cmp_ge_u32 s97, 130
	s_cbranch_scc1 .Lf16_se_L1
	s_add_i32 m0, s96, 0x0
	s_nop 0
	global_load_lds_dwordx4 v170, s[2:3]
	s_add_i32 m0, s96, 0x2000
	s_nop 0
	global_load_lds_dwordx4 v172, s[2:3]
	s_add_i32 m0, s96, 0x4000
	s_nop 0
	global_load_lds_dwordx4 v171, s[2:3]
	s_add_i32 m0, s96, 0x6000
	s_nop 0
	global_load_lds_dwordx4 v173, s[2:3]
	s_add_u32 s2, s2, 0x4000
	s_addc_u32 s3, s3, 0
; #define SBAR() __builtin_amdgcn_sched_barrier(0)
; __device__ __forceinline__ void qkt(f32x16& p0, f32x16& p1, const bf16_t* Ks, const bf16x8* qr, int r32, int hi) {
;   p0 = f32x16{}; p1 = f32x16{};
;   for (int d0 = 0; d0 < 8; ++d0) { int cb = (d0 * 16 + hi * 8) * 2;
;     bf16x8 b0 = *reinterpret_cast<const bf16x8*>((const char*)Ks + KSWZ(r32, cb));
;     bf16x8 b1 = *reinterpret_cast<const bf16x8*>((const char*)Ks + KSWZ(32 + r32, cb));
;     p0 = __builtin_amdgcn_mfma_f32_32x32x16_bf16(b0, qr[d0], p0, 0, 0, 0);
;     p1 = __builtin_amdgcn_mfma_f32_32x32x16_bf16(b1, qr[d0], p1, 0, 0, 0); }
; }
; template <int D0> __device__ __forceinline__ void pv_rd(s16x4 (&r)[8], int vb) {
;   r[0] = tr_read<v_rd_off(D0, 0, 0)>(vb); r[1] = tr_read<v_rd_off(D0, 0, 1)>(vb); r[2] = tr_read<v_rd_off(D0, 1, 0)>(vb); r[3] = tr_read<v_rd_off(D0, 1, 1)>(vb);
;   r[4] = tr_read<v_rd_off(D0, 2, 0)>(vb); r[5] = tr_read<v_rd_off(D0, 2, 1)>(vb); r[6] = tr_read<v_rd_off(D0, 3, 0)>(vb); r[7] = tr_read<v_rd_off(D0, 3, 1)>(vb);
; }
; __device__ __forceinline__ void pv_mm(f32x16& od, const s16x4 (&r)[8], bf16x8 pa0, bf16x8 pa1, bf16x8 pa2, bf16x8 pa3) {
;     ...
;   od = __builtin_amdgcn_mfma_f32_32x32x16_bf16(pa0, PK(r[0], r[1]), od, 0, 0, 0);
;   od = __builtin_amdgcn_mfma_f32_32x32x16_bf16(pa1, PK(r[2], r[3]), od, 0, 0, 0);
;   od = __builtin_amdgcn_mfma_f32_32x32x16_bf16(pa2, PK(r[4], r[5]), od, 0, 0, 0);
;   od = __builtin_amdgcn_mfma_f32_32x32x16_bf16(pa3, PK(r[6], r[7]), od, 0, 0, 0);
;     ...
; }
; __device__ __forceinline__ void pv_d0(f32x16* o, int vb, bf16x8 pa0, bf16x8 pa1, bf16x8 pa2, bf16x8 pa3) {
;   s16x4 ra[8], rb[8];
;   pv_rd<0>(ra, vb); pv_rd<1>(rb, vb);
;   asm volatile("s_waitcnt lgkmcnt(8)" ::: "memory"); SBAR(); pv_mm(o[0], ra, pa0, pa1, pa2, pa3); pv_rd<2>(ra, vb);
;   asm volatile("s_waitcnt lgkmcnt(8)" ::: "memory"); SBAR(); pv_mm(o[1], rb, pa0, pa1, pa2, pa3); pv_rd<3>(rb, vb);
;   asm volatile("s_waitcnt lgkmcnt(8)" ::: "memory"); SBAR(); pv_mm(o[2], ra, pa0, pa1, pa2, pa3);
;   asm volatile("s_waitcnt lgkmcnt(0)" ::: "memory"); SBAR(); pv_mm(o[3], rb, pa0, pa1, pa2, pa3);
; }
.Lf16_se_L1:
	v_cvt_pk_bf16_f32 v130, v66, v67
	v_cvt_pk_bf16_f32 v131, v68, v69
	v_cvt_pk_bf16_f32 v132, v74, v75
	v_cvt_pk_bf16_f32 v133, v76, v77
	v_cvt_pk_bf16_f32 v138, v70, v71
	v_cvt_pk_bf16_f32 v139, v72, v73
	v_cvt_pk_bf16_f32 v140, v78, v79
	v_cvt_pk_bf16_f32 v141, v80, v81
	s_add_i32 s97, s97, 1
	ds_read_b128 v[146:149], v187 offset:32768
	ds_read_b128 v[150:153], v188 offset:32768
	ds_read_b128 v[154:157], v189 offset:32768
	ds_read_b128 v[158:161], v190 offset:32768
	ds_read_b128 v[198:201], v187 offset:36864
	ds_read_b128 v[202:205], v188 offset:36864
	ds_read_b128 v[206:209], v189 offset:36864
	ds_read_b128 v[210:213], v190 offset:36864
	s_waitcnt lgkmcnt(6)
	v_mfma_f32_16x16x32_bf16 v[66:69], v[146:149], v[98:101], 0
	v_exp_f32_e32 v82, v82
	v_mfma_f32_16x16x32_bf16 v[70:73], v[146:149], v[114:117], 0
	v_exp_f32_e32 v83, v83
	v_mfma_f32_16x16x32_bf16 v[66:69], v[150:153], v[102:105], v[66:69]
	v_exp_f32_e32 v84, v84
	v_mfma_f32_16x16x32_bf16 v[70:73], v[150:153], v[118:121], v[70:73]
	v_exp_f32_e32 v85, v85
	ds_read_b128 v[146:149], v187 offset:40960
	ds_read_b128 v[150:153], v188 offset:40960
	s_waitcnt lgkmcnt(6)
	v_mfma_f32_16x16x32_bf16 v[66:69], v[154:157], v[106:109], v[66:69]
	v_exp_f32_e32 v86, v86
	v_mfma_f32_16x16x32_bf16 v[70:73], v[154:157], v[122:125], v[70:73]
	v_exp_f32_e32 v87, v87
	v_mfma_f32_16x16x32_bf16 v[66:69], v[158:161], v[110:113], v[66:69]
	v_exp_f32_e32 v88, v88
	v_mfma_f32_16x16x32_bf16 v[70:73], v[158:161], v[126:129], v[70:73]
	v_exp_f32_e32 v89, v89
	ds_read_b128 v[154:157], v189 offset:40960
	ds_read_b128 v[158:161], v190 offset:40960
	s_waitcnt lgkmcnt(6)
	v_mfma_f32_16x16x32_bf16 v[74:77], v[198:201], v[98:101], 0
	v_exp_f32_e32 v90, v90
	v_mfma_f32_16x16x32_bf16 v[78:81], v[198:201], v[114:117], 0
	v_exp_f32_e32 v91, v91
	v_cvt_pk_bf16_f32 v134, v82, v83
	v_mfma_f32_16x16x32_bf16 v[74:77], v[202:205], v[102:105], v[74:77]
	v_exp_f32_e32 v92, v92
	v_cvt_pk_bf16_f32 v135, v84, v85
	v_mfma_f32_16x16x32_bf16 v[78:81], v[202:205], v[118:121], v[78:81]
	v_exp_f32_e32 v93, v93
	v_cvt_pk_bf16_f32 v142, v86, v87
	ds_read_b128 v[198:201], v187 offset:45056
	ds_read_b128 v[202:205], v188 offset:45056
	s_waitcnt lgkmcnt(6)
	v_mfma_f32_16x16x32_bf16 v[74:77], v[206:209], v[106:109], v[74:77]
	v_exp_f32_e32 v94, v94
	v_cvt_pk_bf16_f32 v143, v88, v89
	v_mfma_f32_16x16x32_bf16 v[78:81], v[206:209], v[122:125], v[78:81]
	v_exp_f32_e32 v95, v95
	v_mfma_f32_16x16x32_bf16 v[74:77], v[210:213], v[110:113], v[74:77]
	v_exp_f32_e32 v96, v96
	v_mfma_f32_16x16x32_bf16 v[78:81], v[210:213], v[126:129], v[78:81]
	v_exp_f32_e32 v97, v97
	ds_read_b128 v[206:209], v189 offset:45056
	ds_read_b128 v[210:213], v190 offset:45056
	s_waitcnt lgkmcnt(6)
	v_mfma_f32_16x16x32_bf16 v[82:85], v[146:149], v[98:101], 0
	v_mfma_f32_16x16x32_bf16 v[86:89], v[146:149], v[114:117], 0
	v_cvt_pk_bf16_f32 v136, v90, v91
	v_mfma_f32_16x16x32_bf16 v[82:85], v[150:153], v[102:105], v[82:85]
	v_cvt_pk_bf16_f32 v137, v92, v93
	v_mfma_f32_16x16x32_bf16 v[86:89], v[150:153], v[118:121], v[86:89]
	v_cvt_pk_bf16_f32 v144, v94, v95
	s_waitcnt lgkmcnt(4)
	v_mfma_f32_16x16x32_bf16 v[82:85], v[154:157], v[106:109], v[82:85]
	v_cvt_pk_bf16_f32 v145, v96, v97
	v_mfma_f32_16x16x32_bf16 v[86:89], v[154:157], v[122:125], v[86:89]
	v_mfma_f32_16x16x32_bf16 v[82:85], v[158:161], v[110:113], v[82:85]
	v_mfma_f32_16x16x32_bf16 v[86:89], v[158:161], v[126:129], v[86:89]
	s_waitcnt lgkmcnt(2)
	v_mfma_f32_16x16x32_bf16 v[90:93], v[198:201], v[98:101], 0
	v_mfma_f32_16x16x32_bf16 v[94:97], v[198:201], v[114:117], 0
	v_mfma_f32_16x16x32_bf16 v[90:93], v[202:205], v[102:105], v[90:93]
	v_mfma_f32_16x16x32_bf16 v[94:97], v[202:205], v[118:121], v[94:97]
	ds_read_b64_tr_b16 v[214:215], v180 offset:0
	ds_read_b64_tr_b16 v[216:217], v180 offset:4096
	ds_read_b64_tr_b16 v[218:219], v181 offset:0
	ds_read_b64_tr_b16 v[220:221], v181 offset:4096
	ds_read_b64_tr_b16 v[222:223], v180 offset:512
	ds_read_b64_tr_b16 v[224:225], v180 offset:4608
	ds_read_b64_tr_b16 v[226:227], v181 offset:512
	ds_read_b64_tr_b16 v[228:229], v181 offset:4608
	ds_read_b64_tr_b16 v[230:231], v180 offset:1024
	ds_read_b64_tr_b16 v[232:233], v180 offset:5120
	ds_read_b64_tr_b16 v[234:235], v181 offset:1024
	ds_read_b64_tr_b16 v[236:237], v181 offset:5120
	s_waitcnt lgkmcnt(12)
	v_mfma_f32_16x16x32_bf16 v[90:93], v[206:209], v[106:109], v[90:93]
	v_mfma_f32_16x16x32_bf16 v[94:97], v[206:209], v[122:125], v[94:97]
	v_mfma_f32_16x16x32_bf16 v[90:93], v[210:213], v[110:113], v[90:93]
	v_mfma_f32_16x16x32_bf16 v[94:97], v[210:213], v[126:129], v[94:97]
	s_waitcnt lgkmcnt(8)
	v_mfma_f32_16x16x32_bf16 v[2:5], v[214:217], v[130:133], v[2:5]
	v_mfma_f32_16x16x32_bf16 v[6:9], v[214:217], v[138:141], v[6:9]
	v_exp_f32_e32 v66, v66
	v_mfma_f32_16x16x32_bf16 v[10:13], v[218:221], v[130:133], v[10:13]
	v_mfma_f32_16x16x32_bf16 v[14:17], v[218:221], v[138:141], v[14:17]
	v_exp_f32_e32 v67, v67
	ds_read_b64_tr_b16 v[238:239], v180 offset:1536
	ds_read_b64_tr_b16 v[240:241], v180 offset:5632
	ds_read_b64_tr_b16 v[242:243], v181 offset:1536
	ds_read_b64_tr_b16 v[244:245], v181 offset:5632
	s_waitcnt lgkmcnt(8)
	v_mfma_f32_16x16x32_bf16 v[18:21], v[222:225], v[130:133], v[18:21]
	v_mfma_f32_16x16x32_bf16 v[22:25], v[222:225], v[138:141], v[22:25]
	v_exp_f32_e32 v68, v68
	v_mfma_f32_16x16x32_bf16 v[26:29], v[226:229], v[130:133], v[26:29]
	v_mfma_f32_16x16x32_bf16 v[30:33], v[226:229], v[138:141], v[30:33]
	v_exp_f32_e32 v69, v69
	v_mfma_f32_16x16x32_bf16 v[246:249], v[194:197], v[130:133], v[246:249]
	ds_read_b64_tr_b16 v[214:215], v180 offset:8192
	ds_read_b64_tr_b16 v[216:217], v180 offset:12288
	ds_read_b64_tr_b16 v[218:219], v181 offset:8192
	ds_read_b64_tr_b16 v[220:221], v181 offset:12288
	s_waitcnt lgkmcnt(8)
; #define SBAR() __builtin_amdgcn_sched_barrier(0)
; #define ATT_SYNC(jn) do { ATT_WAIT_BAR(); if ((jn) < NT) ATT_DMA((jn), (jn) & 3); } while (0)
; template <int D0> __device__ __forceinline__ void pv_rd(s16x4 (&r)[8], int vb) {
;   r[0] = tr_read<v_rd_off(D0, 0, 0)>(vb); r[1] = tr_read<v_rd_off(D0, 0, 1)>(vb); r[2] = tr_read<v_rd_off(D0, 1, 0)>(vb); r[3] = tr_read<v_rd_off(D0, 1, 1)>(vb);
;   r[4] = tr_read<v_rd_off(D0, 2, 0)>(vb); r[5] = tr_read<v_rd_off(D0, 2, 1)>(vb); r[6] = tr_read<v_rd_off(D0, 3, 0)>(vb); r[7] = tr_read<v_rd_off(D0, 3, 1)>(vb);
; }
; __device__ __forceinline__ void pv_mm(f32x16& od, const s16x4 (&r)[8], bf16x8 pa0, bf16x8 pa1, bf16x8 pa2, bf16x8 pa3) {
;     ...
;   od = __builtin_amdgcn_mfma_f32_32x32x16_bf16(pa0, PK(r[0], r[1]), od, 0, 0, 0);
;   od = __builtin_amdgcn_mfma_f32_32x32x16_bf16(pa1, PK(r[2], r[3]), od, 0, 0, 0);
;   od = __builtin_amdgcn_mfma_f32_32x32x16_bf16(pa2, PK(r[4], r[5]), od, 0, 0, 0);
;   od = __builtin_amdgcn_mfma_f32_32x32x16_bf16(pa3, PK(r[6], r[7]), od, 0, 0, 0);
;     ...
; }
; __device__ __forceinline__ void pv_d0(f32x16* o, int vb, bf16x8 pa0, bf16x8 pa1, bf16x8 pa2, bf16x8 pa3) {
;   s16x4 ra[8], rb[8];
;   pv_rd<0>(ra, vb); pv_rd<1>(rb, vb);
;   asm volatile("s_waitcnt lgkmcnt(8)" ::: "memory"); SBAR(); pv_mm(o[0], ra, pa0, pa1, pa2, pa3); pv_rd<2>(ra, vb);
;   asm volatile("s_waitcnt lgkmcnt(8)" ::: "memory"); SBAR(); pv_mm(o[1], rb, pa0, pa1, pa2, pa3); pv_rd<3>(rb, vb);
;   asm volatile("s_waitcnt lgkmcnt(8)" ::: "memory"); SBAR(); pv_mm(o[2], ra, pa0, pa1, pa2, pa3);
;   asm volatile("s_waitcnt lgkmcnt(0)" ::: "memory"); SBAR(); pv_mm(o[3], rb, pa0, pa1, pa2, pa3);
; }
; __device__ __forceinline__ void attn_dma_body(const bf16_t* __restrict__ Qb, int ldq, int tpos0, const float* __restrict__ rope, const float* __restrict__ qgain, ...
;     ...
;   for (int j = 1; j + 1 < NT; j += 2) {
;     { SBAR(); qkt(pB0, pB1, (const bf16_t*)(lds + (j & 3) * SHM_SLOT), qr, r32, hi);
;       finishSM(pA0, pA1, alA, l_reg, pa0, pa1, pa2, pa3); s16x4 va[8]; pv_rd<0>(va, vb0 + ((j - 1) & 3) * (int)SHM_SLOT); SBAR();
;       if (!lead) ATT_SYNC(j + 2);
;       pv_d0_pre(o, vb0 + ((j - 1) & 3) * (int)SHM_SLOT, va, pa0, pa1, pa2, pa3); partialSM(pB0, pB1, m_reg, mnB, alB);
;       if (lead) ATT_SYNC(j + 2);
	v_mfma_f32_16x16x32_bf16 v[34:37], v[230:233], v[130:133], v[34:37]
	v_mfma_f32_16x16x32_bf16 v[38:41], v[230:233], v[138:141], v[38:41]
	v_exp_f32_e32 v70, v70
	v_mfma_f32_16x16x32_bf16 v[42:45], v[234:237], v[130:133], v[42:45]
	v_mfma_f32_16x16x32_bf16 v[46:49], v[234:237], v[138:141], v[46:49]
	v_exp_f32_e32 v71, v71
	ds_read_b64_tr_b16 v[222:223], v180 offset:8704
	ds_read_b64_tr_b16 v[224:225], v180 offset:12800
	ds_read_b64_tr_b16 v[226:227], v181 offset:8704
	ds_read_b64_tr_b16 v[228:229], v181 offset:12800
	s_waitcnt lgkmcnt(8)
	v_mfma_f32_16x16x32_bf16 v[50:53], v[238:241], v[130:133], v[50:53]
	v_mfma_f32_16x16x32_bf16 v[54:57], v[238:241], v[138:141], v[54:57]
	v_exp_f32_e32 v72, v72
	v_mfma_f32_16x16x32_bf16 v[58:61], v[242:245], v[130:133], v[58:61]
	v_mfma_f32_16x16x32_bf16 v[62:65], v[242:245], v[138:141], v[62:65]
	v_exp_f32_e32 v73, v73
	v_mfma_f32_16x16x32_bf16 v[252:255], v[194:197], v[138:141], v[252:255]
	ds_read_b64_tr_b16 v[230:231], v180 offset:9216
	ds_read_b64_tr_b16 v[232:233], v180 offset:13312
	ds_read_b64_tr_b16 v[234:235], v181 offset:9216
	ds_read_b64_tr_b16 v[236:237], v181 offset:13312
	s_waitcnt lgkmcnt(8)
	v_mfma_f32_16x16x32_bf16 v[2:5], v[214:217], v[134:137], v[2:5]
	v_mfma_f32_16x16x32_bf16 v[6:9], v[214:217], v[142:145], v[6:9]
	v_exp_f32_e32 v74, v74
	v_mfma_f32_16x16x32_bf16 v[10:13], v[218:221], v[134:137], v[10:13]
	v_mfma_f32_16x16x32_bf16 v[14:17], v[218:221], v[142:145], v[14:17]
	v_exp_f32_e32 v75, v75
	ds_read_b64_tr_b16 v[238:239], v180 offset:9728
	ds_read_b64_tr_b16 v[240:241], v180 offset:13824
	ds_read_b64_tr_b16 v[242:243], v181 offset:9728
	ds_read_b64_tr_b16 v[244:245], v181 offset:13824
	s_waitcnt lgkmcnt(8)
	v_mfma_f32_16x16x32_bf16 v[18:21], v[222:225], v[134:137], v[18:21]
	v_mfma_f32_16x16x32_bf16 v[22:25], v[222:225], v[142:145], v[22:25]
	v_exp_f32_e32 v76, v76
	v_mfma_f32_16x16x32_bf16 v[26:29], v[226:229], v[134:137], v[26:29]
	v_mfma_f32_16x16x32_bf16 v[30:33], v[226:229], v[142:145], v[30:33]
	v_exp_f32_e32 v77, v77
	v_mfma_f32_16x16x32_bf16 v[246:249], v[194:197], v[134:137], v[246:249]
	s_waitcnt lgkmcnt(4)
	v_mfma_f32_16x16x32_bf16 v[34:37], v[230:233], v[134:137], v[34:37]
	v_mfma_f32_16x16x32_bf16 v[38:41], v[230:233], v[142:145], v[38:41]
	v_exp_f32_e32 v78, v78
	v_mfma_f32_16x16x32_bf16 v[42:45], v[234:237], v[134:137], v[42:45]
	v_mfma_f32_16x16x32_bf16 v[46:49], v[234:237], v[142:145], v[46:49]
	v_exp_f32_e32 v79, v79
	s_waitcnt lgkmcnt(0)
	v_mfma_f32_16x16x32_bf16 v[50:53], v[238:241], v[134:137], v[50:53]
	v_mfma_f32_16x16x32_bf16 v[54:57], v[238:241], v[142:145], v[54:57]
	v_exp_f32_e32 v80, v80
	v_mfma_f32_16x16x32_bf16 v[58:61], v[242:245], v[134:137], v[58:61]
	v_mfma_f32_16x16x32_bf16 v[62:65], v[242:245], v[142:145], v[62:65]
	v_exp_f32_e32 v81, v81
	v_mfma_f32_16x16x32_bf16 v[252:255], v[194:197], v[142:145], v[252:255]
	s_waitcnt vmcnt(0) lgkmcnt(0)
	s_barrier
	s_cmp_ge_u32 s97, 130
	s_cbranch_scc1 .Lf16_se_L2
	s_add_i32 m0, s96, 0x8000
	s_nop 0
	global_load_lds_dwordx4 v170, s[2:3]
	s_add_i32 m0, s96, 0xa000
	s_nop 0
	global_load_lds_dwordx4 v172, s[2:3]
	s_add_i32 m0, s96, 0xc000
	s_nop 0
	global_load_lds_dwordx4 v171, s[2:3]
	s_add_i32 m0, s96, 0xe000
	s_nop 0
	global_load_lds_dwordx4 v173, s[2:3]
	s_add_u32 s2, s2, 0x4000
	s_addc_u32 s3, s3, 0
.Lf16_se_L2:
	v_cvt_pk_bf16_f32 v130, v66, v67
	v_cvt_pk_bf16_f32 v131, v68, v69
	v_cvt_pk_bf16_f32 v132, v74, v75
	v_cvt_pk_bf16_f32 v133, v76, v77
	v_cvt_pk_bf16_f32 v138, v70, v71
	v_cvt_pk_bf16_f32 v139, v72, v73
	v_cvt_pk_bf16_f32 v140, v78, v79
	v_cvt_pk_bf16_f32 v141, v80, v81
	s_add_i32 s97, s97, 1
	s_cmp_lt_u32 s97, 132
	s_cbranch_scc0 .Lf16_done
	ds_read_b128 v[146:149], v183 offset:0
	ds_read_b128 v[150:153], v184 offset:0
	ds_read_b128 v[154:157], v185 offset:0
	ds_read_b128 v[158:161], v186 offset:0
	ds_read_b128 v[198:201], v183 offset:4096
	ds_read_b128 v[202:205], v184 offset:4096
	ds_read_b128 v[206:209], v185 offset:4096
	ds_read_b128 v[210:213], v186 offset:4096
	s_waitcnt lgkmcnt(6)
	v_mfma_f32_16x16x32_bf16 v[66:69], v[146:149], v[98:101], 0
	v_exp_f32_e32 v82, v82
	v_mfma_f32_16x16x32_bf16 v[70:73], v[146:149], v[114:117], 0
	v_exp_f32_e32 v83, v83
	v_mfma_f32_16x16x32_bf16 v[66:69], v[150:153], v[102:105], v[66:69]
	v_exp_f32_e32 v84, v84
	v_mfma_f32_16x16x32_bf16 v[70:73], v[150:153], v[118:121], v[70:73]
	v_exp_f32_e32 v85, v85
	ds_read_b128 v[146:149], v183 offset:8192
	ds_read_b128 v[150:153], v184 offset:8192
	s_waitcnt lgkmcnt(6)
	v_mfma_f32_16x16x32_bf16 v[66:69], v[154:157], v[106:109], v[66:69]
	v_exp_f32_e32 v86, v86
	v_mfma_f32_16x16x32_bf16 v[70:73], v[154:157], v[122:125], v[70:73]
	v_exp_f32_e32 v87, v87
	v_mfma_f32_16x16x32_bf16 v[66:69], v[158:161], v[110:113], v[66:69]
	v_exp_f32_e32 v88, v88
	v_mfma_f32_16x16x32_bf16 v[70:73], v[158:161], v[126:129], v[70:73]
	v_exp_f32_e32 v89, v89
	ds_read_b128 v[154:157], v185 offset:8192
	ds_read_b128 v[158:161], v186 offset:8192
	s_waitcnt lgkmcnt(6)
	v_mfma_f32_16x16x32_bf16 v[74:77], v[198:201], v[98:101], 0
	v_exp_f32_e32 v90, v90
	v_mfma_f32_16x16x32_bf16 v[78:81], v[198:201], v[114:117], 0
	v_exp_f32_e32 v91, v91
	v_cvt_pk_bf16_f32 v134, v82, v83
	v_mfma_f32_16x16x32_bf16 v[74:77], v[202:205], v[102:105], v[74:77]
	v_exp_f32_e32 v92, v92
	v_cvt_pk_bf16_f32 v135, v84, v85
	v_mfma_f32_16x16x32_bf16 v[78:81], v[202:205], v[118:121], v[78:81]
	v_exp_f32_e32 v93, v93
	v_cvt_pk_bf16_f32 v142, v86, v87
	ds_read_b128 v[198:201], v183 offset:12288
	ds_read_b128 v[202:205], v184 offset:12288
	s_waitcnt lgkmcnt(6)
; #define SBAR() __builtin_amdgcn_sched_barrier(0)
; __device__ __forceinline__ void qkt(f32x16& p0, f32x16& p1, const bf16_t* Ks, const bf16x8* qr, int r32, int hi) {
;   p0 = f32x16{}; p1 = f32x16{};
;   for (int d0 = 0; d0 < 8; ++d0) { int cb = (d0 * 16 + hi * 8) * 2;
;     bf16x8 b0 = *reinterpret_cast<const bf16x8*>((const char*)Ks + KSWZ(r32, cb));
;     bf16x8 b1 = *reinterpret_cast<const bf16x8*>((const char*)Ks + KSWZ(32 + r32, cb));
;     p0 = __builtin_amdgcn_mfma_f32_32x32x16_bf16(b0, qr[d0], p0, 0, 0, 0);
;     p1 = __builtin_amdgcn_mfma_f32_32x32x16_bf16(b1, qr[d0], p1, 0, 0, 0); }
; }
; template <int D0> __device__ __forceinline__ void pv_rd(s16x4 (&r)[8], int vb) {
;   r[0] = tr_read<v_rd_off(D0, 0, 0)>(vb); r[1] = tr_read<v_rd_off(D0, 0, 1)>(vb); r[2] = tr_read<v_rd_off(D0, 1, 0)>(vb); r[3] = tr_read<v_rd_off(D0, 1, 1)>(vb);
;   r[4] = tr_read<v_rd_off(D0, 2, 0)>(vb); r[5] = tr_read<v_rd_off(D0, 2, 1)>(vb); r[6] = tr_read<v_rd_off(D0, 3, 0)>(vb); r[7] = tr_read<v_rd_off(D0, 3, 1)>(vb);
; }
; __device__ __forceinline__ void pv_mm(f32x16& od, const s16x4 (&r)[8], bf16x8 pa0, bf16x8 pa1, bf16x8 pa2, bf16x8 pa3) {
;     ...
;   od = __builtin_amdgcn_mfma_f32_32x32x16_bf16(pa0, PK(r[0], r[1]), od, 0, 0, 0);
;   od = __builtin_amdgcn_mfma_f32_32x32x16_bf16(pa1, PK(r[2], r[3]), od, 0, 0, 0);
;   od = __builtin_amdgcn_mfma_f32_32x32x16_bf16(pa2, PK(r[4], r[5]), od, 0, 0, 0);
;   od = __builtin_amdgcn_mfma_f32_32x32x16_bf16(pa3, PK(r[6], r[7]), od, 0, 0, 0);
;     ...
; }
; __device__ __forceinline__ void pv_d0(f32x16* o, int vb, bf16x8 pa0, bf16x8 pa1, bf16x8 pa2, bf16x8 pa3) {
;   s16x4 ra[8], rb[8];
;   pv_rd<0>(ra, vb); pv_rd<1>(rb, vb);
;   asm volatile("s_waitcnt lgkmcnt(8)" ::: "memory"); SBAR(); pv_mm(o[0], ra, pa0, pa1, pa2, pa3); pv_rd<2>(ra, vb);
;   asm volatile("s_waitcnt lgkmcnt(8)" ::: "memory"); SBAR(); pv_mm(o[1], rb, pa0, pa1, pa2, pa3); pv_rd<3>(rb, vb);
;   asm volatile("s_waitcnt lgkmcnt(8)" ::: "memory"); SBAR(); pv_mm(o[2], ra, pa0, pa1, pa2, pa3);
;   asm volatile("s_waitcnt lgkmcnt(0)" ::: "memory"); SBAR(); pv_mm(o[3], rb, pa0, pa1, pa2, pa3);
; }
	v_mfma_f32_16x16x32_bf16 v[74:77], v[206:209], v[106:109], v[74:77]
	v_exp_f32_e32 v94, v94
	v_cvt_pk_bf16_f32 v143, v88, v89
	v_mfma_f32_16x16x32_bf16 v[78:81], v[206:209], v[122:125], v[78:81]
	v_exp_f32_e32 v95, v95
	v_mfma_f32_16x16x32_bf16 v[74:77], v[210:213], v[110:113], v[74:77]
	v_exp_f32_e32 v96, v96
	v_mfma_f32_16x16x32_bf16 v[78:81], v[210:213], v[126:129], v[78:81]
	v_exp_f32_e32 v97, v97
	ds_read_b128 v[206:209], v185 offset:12288
	ds_read_b128 v[210:213], v186 offset:12288
	s_waitcnt lgkmcnt(6)
	v_mfma_f32_16x16x32_bf16 v[82:85], v[146:149], v[98:101], 0
	v_mfma_f32_16x16x32_bf16 v[86:89], v[146:149], v[114:117], 0
	v_cvt_pk_bf16_f32 v136, v90, v91
	v_mfma_f32_16x16x32_bf16 v[82:85], v[150:153], v[102:105], v[82:85]
	v_cvt_pk_bf16_f32 v137, v92, v93
	v_mfma_f32_16x16x32_bf16 v[86:89], v[150:153], v[118:121], v[86:89]
	v_cvt_pk_bf16_f32 v144, v94, v95
	s_waitcnt lgkmcnt(4)
	v_mfma_f32_16x16x32_bf16 v[82:85], v[154:157], v[106:109], v[82:85]
	v_cvt_pk_bf16_f32 v145, v96, v97
	v_mfma_f32_16x16x32_bf16 v[86:89], v[154:157], v[122:125], v[86:89]
	v_mfma_f32_16x16x32_bf16 v[82:85], v[158:161], v[110:113], v[82:85]
	v_mfma_f32_16x16x32_bf16 v[86:89], v[158:161], v[126:129], v[86:89]
	s_waitcnt lgkmcnt(2)
	v_mfma_f32_16x16x32_bf16 v[90:93], v[198:201], v[98:101], 0
	v_mfma_f32_16x16x32_bf16 v[94:97], v[198:201], v[114:117], 0
	v_mfma_f32_16x16x32_bf16 v[90:93], v[202:205], v[102:105], v[90:93]
	v_mfma_f32_16x16x32_bf16 v[94:97], v[202:205], v[118:121], v[94:97]
	ds_read_b64_tr_b16 v[214:215], v180 offset:32768
	ds_read_b64_tr_b16 v[216:217], v180 offset:36864
	ds_read_b64_tr_b16 v[218:219], v181 offset:32768
	ds_read_b64_tr_b16 v[220:221], v181 offset:36864
	ds_read_b64_tr_b16 v[222:223], v180 offset:33280
	ds_read_b64_tr_b16 v[224:225], v180 offset:37376
	ds_read_b64_tr_b16 v[226:227], v181 offset:33280
	ds_read_b64_tr_b16 v[228:229], v181 offset:37376
	ds_read_b64_tr_b16 v[230:231], v180 offset:33792
	ds_read_b64_tr_b16 v[232:233], v180 offset:37888
	ds_read_b64_tr_b16 v[234:235], v181 offset:33792
	ds_read_b64_tr_b16 v[236:237], v181 offset:37888
	s_waitcnt lgkmcnt(12)
	v_mfma_f32_16x16x32_bf16 v[90:93], v[206:209], v[106:109], v[90:93]
	v_mfma_f32_16x16x32_bf16 v[94:97], v[206:209], v[122:125], v[94:97]
	v_mfma_f32_16x16x32_bf16 v[90:93], v[210:213], v[110:113], v[90:93]
	v_mfma_f32_16x16x32_bf16 v[94:97], v[210:213], v[126:129], v[94:97]
	s_waitcnt lgkmcnt(8)
	v_mfma_f32_16x16x32_bf16 v[2:5], v[214:217], v[130:133], v[2:5]
	v_mfma_f32_16x16x32_bf16 v[6:9], v[214:217], v[138:141], v[6:9]
	v_exp_f32_e32 v66, v66
	v_mfma_f32_16x16x32_bf16 v[10:13], v[218:221], v[130:133], v[10:13]
	v_mfma_f32_16x16x32_bf16 v[14:17], v[218:221], v[138:141], v[14:17]
	v_exp_f32_e32 v67, v67
	ds_read_b64_tr_b16 v[238:239], v180 offset:34304
	ds_read_b64_tr_b16 v[240:241], v180 offset:38400
	ds_read_b64_tr_b16 v[242:243], v181 offset:34304
	ds_read_b64_tr_b16 v[244:245], v181 offset:38400
	s_waitcnt lgkmcnt(8)
	v_mfma_f32_16x16x32_bf16 v[18:21], v[222:225], v[130:133], v[18:21]
	v_mfma_f32_16x16x32_bf16 v[22:25], v[222:225], v[138:141], v[22:25]
	v_exp_f32_e32 v68, v68
	v_mfma_f32_16x16x32_bf16 v[26:29], v[226:229], v[130:133], v[26:29]
	v_mfma_f32_16x16x32_bf16 v[30:33], v[226:229], v[138:141], v[30:33]
	v_exp_f32_e32 v69, v69
	v_mfma_f32_16x16x32_bf16 v[246:249], v[194:197], v[130:133], v[246:249]
	ds_read_b64_tr_b16 v[214:215], v180 offset:40960
	ds_read_b64_tr_b16 v[216:217], v180 offset:45056
	ds_read_b64_tr_b16 v[218:219], v181 offset:40960
	ds_read_b64_tr_b16 v[220:221], v181 offset:45056
	s_waitcnt lgkmcnt(8)
	v_mfma_f32_16x16x32_bf16 v[34:37], v[230:233], v[130:133], v[34:37]
	v_mfma_f32_16x16x32_bf16 v[38:41], v[230:233], v[138:141], v[38:41]
	v_exp_f32_e32 v70, v70
	v_mfma_f32_16x16x32_bf16 v[42:45], v[234:237], v[130:133], v[42:45]
	v_mfma_f32_16x16x32_bf16 v[46:49], v[234:237], v[138:141], v[46:49]
	v_exp_f32_e32 v71, v71
	ds_read_b64_tr_b16 v[222:223], v180 offset:41472
	ds_read_b64_tr_b16 v[224:225], v180 offset:45568
	ds_read_b64_tr_b16 v[226:227], v181 offset:41472
	ds_read_b64_tr_b16 v[228:229], v181 offset:45568
	s_waitcnt lgkmcnt(8)
	v_mfma_f32_16x16x32_bf16 v[50:53], v[238:241], v[130:133], v[50:53]
	v_mfma_f32_16x16x32_bf16 v[54:57], v[238:241], v[138:141], v[54:57]
	v_exp_f32_e32 v72, v72
	v_mfma_f32_16x16x32_bf16 v[58:61], v[242:245], v[130:133], v[58:61]
	v_mfma_f32_16x16x32_bf16 v[62:65], v[242:245], v[138:141], v[62:65]
	v_exp_f32_e32 v73, v73
	v_mfma_f32_16x16x32_bf16 v[252:255], v[194:197], v[138:141], v[252:255]
	ds_read_b64_tr_b16 v[230:231], v180 offset:41984
	ds_read_b64_tr_b16 v[232:233], v180 offset:46080
	ds_read_b64_tr_b16 v[234:235], v181 offset:41984
	ds_read_b64_tr_b16 v[236:237], v181 offset:46080
	s_waitcnt lgkmcnt(8)
	v_mfma_f32_16x16x32_bf16 v[2:5], v[214:217], v[134:137], v[2:5]
	v_mfma_f32_16x16x32_bf16 v[6:9], v[214:217], v[142:145], v[6:9]
	v_exp_f32_e32 v74, v74
	v_mfma_f32_16x16x32_bf16 v[10:13], v[218:221], v[134:137], v[10:13]
	v_mfma_f32_16x16x32_bf16 v[14:17], v[218:221], v[142:145], v[14:17]
	v_exp_f32_e32 v75, v75
	ds_read_b64_tr_b16 v[238:239], v180 offset:42496
	ds_read_b64_tr_b16 v[240:241], v180 offset:46592
	ds_read_b64_tr_b16 v[242:243], v181 offset:42496
	ds_read_b64_tr_b16 v[244:245], v181 offset:46592
	s_waitcnt lgkmcnt(8)
	v_mfma_f32_16x16x32_bf16 v[18:21], v[222:225], v[134:137], v[18:21]
	v_mfma_f32_16x16x32_bf16 v[22:25], v[222:225], v[142:145], v[22:25]
	v_exp_f32_e32 v76, v76
	v_mfma_f32_16x16x32_bf16 v[26:29], v[226:229], v[134:137], v[26:29]
	v_mfma_f32_16x16x32_bf16 v[30:33], v[226:229], v[142:145], v[30:33]
	v_exp_f32_e32 v77, v77
	v_mfma_f32_16x16x32_bf16 v[246:249], v[194:197], v[134:137], v[246:249]
	s_waitcnt lgkmcnt(4)
	v_mfma_f32_16x16x32_bf16 v[34:37], v[230:233], v[134:137], v[34:37]
	v_mfma_f32_16x16x32_bf16 v[38:41], v[230:233], v[142:145], v[38:41]
	v_exp_f32_e32 v78, v78
	v_mfma_f32_16x16x32_bf16 v[42:45], v[234:237], v[134:137], v[42:45]
	v_mfma_f32_16x16x32_bf16 v[46:49], v[234:237], v[142:145], v[46:49]
	v_exp_f32_e32 v79, v79
	s_waitcnt lgkmcnt(0)
	v_mfma_f32_16x16x32_bf16 v[50:53], v[238:241], v[134:137], v[50:53]
	v_mfma_f32_16x16x32_bf16 v[54:57], v[238:241], v[142:145], v[54:57]
	v_exp_f32_e32 v80, v80
	v_mfma_f32_16x16x32_bf16 v[58:61], v[242:245], v[134:137], v[58:61]
	v_mfma_f32_16x16x32_bf16 v[62:65], v[242:245], v[142:145], v[62:65]
	v_exp_f32_e32 v81, v81
	v_mfma_f32_16x16x32_bf16 v[252:255], v[194:197], v[142:145], v[252:255]
	s_waitcnt vmcnt(0) lgkmcnt(0)
	s_barrier
	s_cmp_ge_u32 s97, 130
	s_cbranch_scc1 .Lf16_se_L3
	s_add_i32 m0, s96, 0x10000
	s_nop 0
	global_load_lds_dwordx4 v170, s[2:3]
	s_add_i32 m0, s96, 0x12000
	s_nop 0
	global_load_lds_dwordx4 v172, s[2:3]
	s_add_i32 m0, s96, 0x14000
	s_nop 0
	global_load_lds_dwordx4 v171, s[2:3]
	s_add_i32 m0, s96, 0x16000
	s_nop 0
	global_load_lds_dwordx4 v173, s[2:3]
	s_add_u32 s2, s2, 0x4000
	s_addc_u32 s3, s3, 0
; #define SBAR() __builtin_amdgcn_sched_barrier(0)
; __device__ __forceinline__ int crow(int r, int hi) { return (r & 3) + 8 * (r >> 2) + 4 * hi; }
; #define RESC(a) do { if (__any((a) < 1.f)) { if (hi == 0) al_l[r32] = (a); asm volatile("s_waitcnt lgkmcnt(0)" ::: "memory"); \
;     for (int d = 0; d < 4; ++d) for (int r = 0; r < 16; ++r) o[d][r] *= al_l[crow(r, hi)]; } } while (0)
; #define RESC(a) do { if (__any((a) < 1.f)) { if (hi == 0) al_l[r32] = (a); asm volatile("s_waitcnt lgkmcnt(0)" ::: "memory"); \
;     for (int d = 0; d < 4; ++d) for (int r = 0; r < 16; ++r) o[d][r] *= al_l[crow(r, hi)]; } } while (0)
; __device__ __forceinline__ void attn_dma_body(const bf16_t* __restrict__ Qb, int ldq, int tpos0, const float* __restrict__ rope, const float* __restrict__ qgain, ...
;     ...
;   { SBAR(); qkt(pB0, pB1, (const bf16_t*)(lds + ((NT - 1) & 3) * SHM_SLOT), qr, r32, hi);
;     finishSM(pA0, pA1, alA, l_reg, pa0, pa1, pa2, pa3); SBAR();
;     pv_d0(o, vb0 + ((NT - 2) & 3) * (int)SHM_SLOT, pa0, pa1, pa2, pa3); partialSM(pB0, pB1, m_reg, mnB, alB);
;     RESC(alB);
;     finishSM(pB0, pB1, alB, l_reg, pa0, pa1, pa2, pa3); SBAR();
;     pv_d0(o, vb0 + ((NT - 1) & 3) * (int)SHM_SLOT, pa0, pa1, pa2, pa3); }
;   if (hi == 0) li_l[r32] = l_reg; asm volatile("s_waitcnt lgkmcnt(0)" ::: "memory");
;   float rli[16];
; #pragma unroll
;   for (int r = 0; r < 16; ++r) rli[r] = __builtin_amdgcn_rcpf(li_l[crow(r, hi)]);
;   bf16_t* Ow = Ob + (long)(wid * QBLK) * LDO;
;   asm volatile("s_waitcnt lgkmcnt(0)\n\ts_barrier" ::: "memory");
.Lf16_se_L3:
	v_cvt_pk_bf16_f32 v130, v66, v67
	v_cvt_pk_bf16_f32 v131, v68, v69
	v_cvt_pk_bf16_f32 v132, v74, v75
	v_cvt_pk_bf16_f32 v133, v76, v77
	v_cvt_pk_bf16_f32 v138, v70, v71
	v_cvt_pk_bf16_f32 v139, v72, v73
	v_cvt_pk_bf16_f32 v140, v78, v79
	v_cvt_pk_bf16_f32 v141, v80, v81
	s_add_i32 s97, s97, 1
	s_branch .Lf16_L_loop
.Lf16_done:
	v_exp_f32_e32 v82, v82
	v_exp_f32_e32 v83, v83
	v_exp_f32_e32 v84, v84
	v_exp_f32_e32 v85, v85
	v_exp_f32_e32 v86, v86
	v_exp_f32_e32 v87, v87
	v_exp_f32_e32 v88, v88
	v_exp_f32_e32 v89, v89
	v_exp_f32_e32 v90, v90
	v_exp_f32_e32 v91, v91
	v_cvt_pk_bf16_f32 v134, v82, v83
	v_exp_f32_e32 v92, v92
	v_cvt_pk_bf16_f32 v135, v84, v85
	v_exp_f32_e32 v93, v93
	v_cvt_pk_bf16_f32 v142, v86, v87
	v_exp_f32_e32 v94, v94
	v_cvt_pk_bf16_f32 v143, v88, v89
	v_exp_f32_e32 v95, v95
	v_exp_f32_e32 v96, v96
	v_exp_f32_e32 v97, v97
	v_cvt_pk_bf16_f32 v136, v90, v91
	v_cvt_pk_bf16_f32 v137, v92, v93
	v_cvt_pk_bf16_f32 v144, v94, v95
	v_cvt_pk_bf16_f32 v145, v96, v97
	s_mov_b32 s37, 0x18000
	ds_read_b64_tr_b16 v[214:215], v180 offset:32768
	ds_read_b64_tr_b16 v[216:217], v180 offset:36864
	ds_read_b64_tr_b16 v[218:219], v181 offset:32768
	ds_read_b64_tr_b16 v[220:221], v181 offset:36864
	ds_read_b64_tr_b16 v[222:223], v180 offset:33280
	ds_read_b64_tr_b16 v[224:225], v180 offset:37376
	ds_read_b64_tr_b16 v[226:227], v181 offset:33280
	ds_read_b64_tr_b16 v[228:229], v181 offset:37376
	ds_read_b64_tr_b16 v[230:231], v180 offset:33792
	ds_read_b64_tr_b16 v[232:233], v180 offset:37888
	ds_read_b64_tr_b16 v[234:235], v181 offset:33792
	ds_read_b64_tr_b16 v[236:237], v181 offset:37888
	s_waitcnt lgkmcnt(8)
	v_mfma_f32_16x16x32_bf16 v[2:5], v[214:217], v[130:133], v[2:5]
	v_mfma_f32_16x16x32_bf16 v[6:9], v[214:217], v[138:141], v[6:9]
	v_mfma_f32_16x16x32_bf16 v[10:13], v[218:221], v[130:133], v[10:13]
	v_mfma_f32_16x16x32_bf16 v[14:17], v[218:221], v[138:141], v[14:17]
	ds_read_b64_tr_b16 v[238:239], v180 offset:34304
	ds_read_b64_tr_b16 v[240:241], v180 offset:38400
	ds_read_b64_tr_b16 v[242:243], v181 offset:34304
	ds_read_b64_tr_b16 v[244:245], v181 offset:38400
	s_waitcnt lgkmcnt(8)
	v_mfma_f32_16x16x32_bf16 v[18:21], v[222:225], v[130:133], v[18:21]
	v_mfma_f32_16x16x32_bf16 v[22:25], v[222:225], v[138:141], v[22:25]
	v_mfma_f32_16x16x32_bf16 v[26:29], v[226:229], v[130:133], v[26:29]
	v_mfma_f32_16x16x32_bf16 v[30:33], v[226:229], v[138:141], v[30:33]
	v_mfma_f32_16x16x32_bf16 v[246:249], v[194:197], v[130:133], v[246:249]
	ds_read_b64_tr_b16 v[214:215], v180 offset:40960
	ds_read_b64_tr_b16 v[216:217], v180 offset:45056
	ds_read_b64_tr_b16 v[218:219], v181 offset:40960
	ds_read_b64_tr_b16 v[220:221], v181 offset:45056
	s_waitcnt lgkmcnt(8)
	v_mfma_f32_16x16x32_bf16 v[34:37], v[230:233], v[130:133], v[34:37]
	v_mfma_f32_16x16x32_bf16 v[38:41], v[230:233], v[138:141], v[38:41]
	v_mfma_f32_16x16x32_bf16 v[42:45], v[234:237], v[130:133], v[42:45]
	v_mfma_f32_16x16x32_bf16 v[46:49], v[234:237], v[138:141], v[46:49]
	ds_read_b64_tr_b16 v[222:223], v180 offset:41472
	ds_read_b64_tr_b16 v[224:225], v180 offset:45568
	ds_read_b64_tr_b16 v[226:227], v181 offset:41472
	ds_read_b64_tr_b16 v[228:229], v181 offset:45568
	s_waitcnt lgkmcnt(8)
	v_mfma_f32_16x16x32_bf16 v[50:53], v[238:241], v[130:133], v[50:53]
	v_mfma_f32_16x16x32_bf16 v[54:57], v[238:241], v[138:141], v[54:57]
	v_mfma_f32_16x16x32_bf16 v[58:61], v[242:245], v[130:133], v[58:61]
	v_mfma_f32_16x16x32_bf16 v[62:65], v[242:245], v[138:141], v[62:65]
	v_mfma_f32_16x16x32_bf16 v[252:255], v[194:197], v[138:141], v[252:255]
	ds_read_b64_tr_b16 v[230:231], v180 offset:41984
	ds_read_b64_tr_b16 v[232:233], v180 offset:46080
	ds_read_b64_tr_b16 v[234:235], v181 offset:41984
	ds_read_b64_tr_b16 v[236:237], v181 offset:46080
	s_waitcnt lgkmcnt(8)
	v_mfma_f32_16x16x32_bf16 v[2:5], v[214:217], v[134:137], v[2:5]
	v_mfma_f32_16x16x32_bf16 v[6:9], v[214:217], v[142:145], v[6:9]
	v_mfma_f32_16x16x32_bf16 v[10:13], v[218:221], v[134:137], v[10:13]
	v_mfma_f32_16x16x32_bf16 v[14:17], v[218:221], v[142:145], v[14:17]
	ds_read_b64_tr_b16 v[238:239], v180 offset:42496
	ds_read_b64_tr_b16 v[240:241], v180 offset:46592
	ds_read_b64_tr_b16 v[242:243], v181 offset:42496
	ds_read_b64_tr_b16 v[244:245], v181 offset:46592
	s_waitcnt lgkmcnt(8)
	v_mfma_f32_16x16x32_bf16 v[18:21], v[222:225], v[134:137], v[18:21]
	v_mfma_f32_16x16x32_bf16 v[22:25], v[222:225], v[142:145], v[22:25]
	v_mfma_f32_16x16x32_bf16 v[26:29], v[226:229], v[134:137], v[26:29]
	v_mfma_f32_16x16x32_bf16 v[30:33], v[226:229], v[142:145], v[30:33]
	v_mfma_f32_16x16x32_bf16 v[246:249], v[194:197], v[134:137], v[246:249]
	s_waitcnt lgkmcnt(4)
	v_mfma_f32_16x16x32_bf16 v[34:37], v[230:233], v[134:137], v[34:37]
	v_mfma_f32_16x16x32_bf16 v[38:41], v[230:233], v[142:145], v[38:41]
	v_mfma_f32_16x16x32_bf16 v[42:45], v[234:237], v[134:137], v[42:45]
	v_mfma_f32_16x16x32_bf16 v[46:49], v[234:237], v[142:145], v[46:49]
	s_waitcnt lgkmcnt(0)
	v_mfma_f32_16x16x32_bf16 v[50:53], v[238:241], v[134:137], v[50:53]
	v_mfma_f32_16x16x32_bf16 v[54:57], v[238:241], v[142:145], v[54:57]
	v_mfma_f32_16x16x32_bf16 v[58:61], v[242:245], v[134:137], v[58:61]
	v_mfma_f32_16x16x32_bf16 v[62:65], v[242:245], v[142:145], v[62:65]
	v_mfma_f32_16x16x32_bf16 v[252:255], v[194:197], v[142:145], v[252:255]
	s_nop 7
	s_nop 7
	v_mov_b32_e32 v182, v246
	v_mov_b32_e32 v195, v252
	v_rcp_f32_e32 v182, v182
	v_rcp_f32_e32 v195, v195
	s_waitcnt lgkmcnt(0)
	s_barrier
; __device__ __forceinline__ unsigned f2bf(float f) { unsigned u = __builtin_bit_cast(unsigned, f); return (u + 0x7fffu + ((u >> 16) & 1u)) >> 16; }
; __device__ __forceinline__ int crow(int r, int hi) { return (r & 3) + 8 * (r >> 2) + 4 * hi; }
; #define ATT_WAIT_BAR() asm volatile("s_waitcnt vmcnt(0) lgkmcnt(0)\n\ts_barrier" ::: "memory")
; __device__ __forceinline__ void attn_dma_body(const bf16_t* __restrict__ Qb, int ldq, int tpos0, const float* __restrict__ rope, const float* __restrict__ qgain, ...
;     ...
;   if (hi == 0) li_l[r32] = l_reg; asm volatile("s_waitcnt lgkmcnt(0)" ::: "memory");
;   float rli[16];
; #pragma unroll
;   for (int r = 0; r < 16; ++r) rli[r] = __builtin_amdgcn_rcpf(li_l[crow(r, hi)]);
;   bf16_t* Ow = Ob + (long)(wid * QBLK) * LDO;
;   asm volatile("s_waitcnt lgkmcnt(0)\n\ts_barrier" ::: "memory");
;   { char* st = lds + wid * 8704;
; #pragma unroll
;     for (int r = 0; r < 16; ++r) { const int orow = crow(r, hi);
; #pragma unroll
;       for (int d0 = 0; d0 < 4; ++d0) *(bf16_t*)(st + orow * 272 + (d0 * 32 + r32) * 2) = (bf16_t)f2bf(o[d0][r] * rli[r]); }
;     asm volatile("s_waitcnt lgkmcnt(0)" ::: "memory");
; #pragma unroll
;     for (int i = 0; i < 8; ++i) { const int c = i * 64 + lane, row = c >> 4, cc = c & 15; const u32x4 v = *(const u32x4*)(st + row * 272 + cc * 16);
;       const bf16_t* gp = Ow + (long)row * LDO + cc * 8;
;       asm volatile("global_store_dwordx4 %0, %1, off sc1\n\ts_nop 1" :: "v"(gp), "v"(v) : "memory"); } }
;   ATT_WAIT_BAR();
	v_mul_u32_u24_e32 v84, 0x2200, v179
	v_and_b32_e32 v246, 15, v167
	v_lshrrev_b32_e32 v247, 4, v167
	v_mul_u32_u24_e32 v248, 0x110, v246
	v_add_u32_e32 v248, v248, v84
	v_lshl_add_u32 v248, v247, 3, v248
	v_mul_f32_e32 v2, v2, v182
	v_mul_f32_e32 v3, v3, v182
	v_mul_f32_e32 v4, v4, v182
	v_mul_f32_e32 v5, v5, v182
	v_cvt_pk_bf16_f32 v252, v2, v3
	v_cvt_pk_bf16_f32 v253, v4, v5
	ds_write_b64 v248, v[252:253] offset:0
	v_mul_f32_e32 v6, v6, v195
	v_mul_f32_e32 v7, v7, v195
	v_mul_f32_e32 v8, v8, v195
	v_mul_f32_e32 v9, v9, v195
	v_cvt_pk_bf16_f32 v254, v6, v7
	v_cvt_pk_bf16_f32 v255, v8, v9
	ds_write_b64 v248, v[254:255] offset:4352
	v_mul_f32_e32 v10, v10, v182
	v_mul_f32_e32 v11, v11, v182
	v_mul_f32_e32 v12, v12, v182
	v_mul_f32_e32 v13, v13, v182
	v_cvt_pk_bf16_f32 v252, v10, v11
	v_cvt_pk_bf16_f32 v253, v12, v13
	ds_write_b64 v248, v[252:253] offset:32
	v_mul_f32_e32 v14, v14, v195
	v_mul_f32_e32 v15, v15, v195
	v_mul_f32_e32 v16, v16, v195
	v_mul_f32_e32 v17, v17, v195
	v_cvt_pk_bf16_f32 v254, v14, v15
	v_cvt_pk_bf16_f32 v255, v16, v17
	ds_write_b64 v248, v[254:255] offset:4384
	v_mul_f32_e32 v18, v18, v182
	v_mul_f32_e32 v19, v19, v182
	v_mul_f32_e32 v20, v20, v182
	v_mul_f32_e32 v21, v21, v182
	v_cvt_pk_bf16_f32 v252, v18, v19
	v_cvt_pk_bf16_f32 v253, v20, v21
	ds_write_b64 v248, v[252:253] offset:64
	v_mul_f32_e32 v22, v22, v195
	v_mul_f32_e32 v23, v23, v195
	v_mul_f32_e32 v24, v24, v195
	v_mul_f32_e32 v25, v25, v195
	v_cvt_pk_bf16_f32 v254, v22, v23
	v_cvt_pk_bf16_f32 v255, v24, v25
	ds_write_b64 v248, v[254:255] offset:4416
	v_mul_f32_e32 v26, v26, v182
	v_mul_f32_e32 v27, v27, v182
	v_mul_f32_e32 v28, v28, v182
	v_mul_f32_e32 v29, v29, v182
	v_cvt_pk_bf16_f32 v252, v26, v27
	v_cvt_pk_bf16_f32 v253, v28, v29
	ds_write_b64 v248, v[252:253] offset:96
	v_mul_f32_e32 v30, v30, v195
	v_mul_f32_e32 v31, v31, v195
	v_mul_f32_e32 v32, v32, v195
	v_mul_f32_e32 v33, v33, v195
	v_cvt_pk_bf16_f32 v254, v30, v31
	v_cvt_pk_bf16_f32 v255, v32, v33
	ds_write_b64 v248, v[254:255] offset:4448
	v_mul_f32_e32 v34, v34, v182
	v_mul_f32_e32 v35, v35, v182
	v_mul_f32_e32 v36, v36, v182
	v_mul_f32_e32 v37, v37, v182
	v_cvt_pk_bf16_f32 v252, v34, v35
	v_cvt_pk_bf16_f32 v253, v36, v37
	ds_write_b64 v248, v[252:253] offset:128
	v_mul_f32_e32 v38, v38, v195
	v_mul_f32_e32 v39, v39, v195
	v_mul_f32_e32 v40, v40, v195
	v_mul_f32_e32 v41, v41, v195
	v_cvt_pk_bf16_f32 v254, v38, v39
	v_cvt_pk_bf16_f32 v255, v40, v41
	ds_write_b64 v248, v[254:255] offset:4480
	v_mul_f32_e32 v42, v42, v182
	v_mul_f32_e32 v43, v43, v182
	v_mul_f32_e32 v44, v44, v182
	v_mul_f32_e32 v45, v45, v182
	v_cvt_pk_bf16_f32 v252, v42, v43
	v_cvt_pk_bf16_f32 v253, v44, v45
	ds_write_b64 v248, v[252:253] offset:160
	v_mul_f32_e32 v46, v46, v195
	v_mul_f32_e32 v47, v47, v195
	v_mul_f32_e32 v48, v48, v195
	v_mul_f32_e32 v49, v49, v195
	v_cvt_pk_bf16_f32 v254, v46, v47
	v_cvt_pk_bf16_f32 v255, v48, v49
	ds_write_b64 v248, v[254:255] offset:4512
	v_mul_f32_e32 v50, v50, v182
	v_mul_f32_e32 v51, v51, v182
	v_mul_f32_e32 v52, v52, v182
	v_mul_f32_e32 v53, v53, v182
	v_cvt_pk_bf16_f32 v252, v50, v51
	v_cvt_pk_bf16_f32 v253, v52, v53
	ds_write_b64 v248, v[252:253] offset:192
	v_mul_f32_e32 v54, v54, v195
	v_mul_f32_e32 v55, v55, v195
	v_mul_f32_e32 v56, v56, v195
	v_mul_f32_e32 v57, v57, v195
	v_cvt_pk_bf16_f32 v254, v54, v55
	v_cvt_pk_bf16_f32 v255, v56, v57
	ds_write_b64 v248, v[254:255] offset:4544
	v_mul_f32_e32 v58, v58, v182
	v_mul_f32_e32 v59, v59, v182
	v_mul_f32_e32 v60, v60, v182
	v_mul_f32_e32 v61, v61, v182
	v_cvt_pk_bf16_f32 v252, v58, v59
	v_cvt_pk_bf16_f32 v253, v60, v61
	ds_write_b64 v248, v[252:253] offset:224
	v_mul_f32_e32 v62, v62, v195
	v_mul_f32_e32 v63, v63, v195
	v_mul_f32_e32 v64, v64, v195
	v_mul_f32_e32 v65, v65, v195
	v_cvt_pk_bf16_f32 v254, v62, v63
	v_cvt_pk_bf16_f32 v255, v64, v65
	ds_write_b64 v248, v[254:255] offset:4576
	s_waitcnt lgkmcnt(0)
	s_lshl_b64 s[6:7], s[70:71], 12
	s_add_u32 s6, s23, s6
	s_addc_u32 s7, s94, s7
	s_add_u32 s6, s6, s44
	s_addc_u32 s7, s7, s45
	v_ashrrev_i32_e32 v165, 31, v164
	v_lshlrev_b64 v[66:67], 12, v[164:165]
	v_lshl_add_u64 v[6:7], s[6:7], 0, v[66:67]
	v_lshlrev_b32_e32 v162, 4, v246
	v_lshl_add_u64 v[6:7], v[6:7], 0, v[162:163]
	v_lshlrev_b32_e32 v162, 12, v247
	v_lshl_add_u64 v[6:7], v[6:7], 0, v[162:163]
	v_mul_u32_u24_e32 v249, 0x110, v247
	v_add_u32_e32 v249, v249, v84
	v_lshl_add_u32 v249, v246, 4, v249
	ds_read_b128 v[10:13], v249 offset:0
	s_mov_b64 s[8:9], 0x0
	v_lshl_add_u64 v[8:9], v[6:7], 0, s[8:9]
	s_waitcnt lgkmcnt(0)
	global_store_dwordx4 v[8:9], v[10:13], off sc1
	s_nop 1
	ds_read_b128 v[14:17], v249 offset:1088
	s_mov_b64 s[8:9], 0x4000
	v_lshl_add_u64 v[8:9], v[6:7], 0, s[8:9]
	s_waitcnt lgkmcnt(0)
	global_store_dwordx4 v[8:9], v[14:17], off sc1
	s_nop 1
	ds_read_b128 v[10:13], v249 offset:2176
	s_mov_b64 s[8:9], 0x8000
	v_lshl_add_u64 v[8:9], v[6:7], 0, s[8:9]
	s_waitcnt lgkmcnt(0)
	global_store_dwordx4 v[8:9], v[10:13], off sc1
	s_nop 1
	ds_read_b128 v[14:17], v249 offset:3264
	s_mov_b64 s[8:9], 0xc000
	v_lshl_add_u64 v[8:9], v[6:7], 0, s[8:9]
	s_waitcnt lgkmcnt(0)
	global_store_dwordx4 v[8:9], v[14:17], off sc1
	s_nop 1
	ds_read_b128 v[10:13], v249 offset:4352
	s_mov_b64 s[8:9], 0x10000
	v_lshl_add_u64 v[8:9], v[6:7], 0, s[8:9]
	s_waitcnt lgkmcnt(0)
	global_store_dwordx4 v[8:9], v[10:13], off sc1
	s_nop 1
	ds_read_b128 v[14:17], v249 offset:5440
	s_mov_b64 s[8:9], 0x14000
	v_lshl_add_u64 v[8:9], v[6:7], 0, s[8:9]
	s_waitcnt lgkmcnt(0)
	global_store_dwordx4 v[8:9], v[14:17], off sc1
	s_nop 1
	ds_read_b128 v[10:13], v249 offset:6528
	s_mov_b64 s[8:9], 0x18000
	v_lshl_add_u64 v[8:9], v[6:7], 0, s[8:9]
	s_waitcnt lgkmcnt(0)
	global_store_dwordx4 v[8:9], v[10:13], off sc1
	s_nop 1
	ds_read_b128 v[14:17], v249 offset:7616
	s_mov_b64 s[8:9], 0x1c000
	v_lshl_add_u64 v[8:9], v[6:7], 0, s[8:9]
	s_waitcnt lgkmcnt(0)
	global_store_dwordx4 v[8:9], v[14:17], off sc1
	s_nop 1
	s_waitcnt vmcnt(0) lgkmcnt(0)
	s_barrier
	v_readlane_b32 s96, v250, 4
	v_readlane_b32 s97, v250, 5
	s_setprio 0
	s_branch .LBB0_437
